# v049 resume: re-measure after sandbox loss (same file as v049)
# speedup vs baseline: 1.0080x; 1.0080x over previous
.LBB0_60:
	s_mov_b32 s17, s35
	s_mov_b32 s24, s70
	s_mov_b32 s16, s34
	s_mov_b32 s22, s26
	s_mov_b32 s23, s27
	s_mov_b32 s21, s25
	s_mov_b64 s[18:19], s[68:69]
	s_mov_b64 s[30:31], -1
	s_mov_b64 s[2:3], 0
	s_cmp_lt_i32 s35, 2
	s_mov_b64 s[28:29], 0
	s_cbranch_scc1 .LBB0_67
	s_cmp_eq_u32 s17, 2
	s_mov_b64 s[28:29], -1
	s_cbranch_scc0 .LBB0_63
	s_waitcnt vmcnt(0)
	v_mov_b32_e32 v88, 0x4b400000
	v_mov_b32_e32 v89, 0x4b40007f
	v_mov_b32_e32 v90, 0x4b3fff81
	v_mov_b32_e32 v91, 0xc0c0400
	v_add_u32_e32 v72, v78, v77
	v_fmamk_f32 v2, v2, 0x44800000, v88
	v_fmamk_f32 v6, v6, 0x44800000, v88
	v_fmamk_f32 v10, v10, 0x44800000, v88
	v_fmamk_f32 v14, v14, 0x44800000, v88
	v_med3_f32 v2, v2, v90, v89
	v_med3_f32 v6, v6, v90, v89
	v_med3_f32 v10, v10, v90, v89
	v_med3_f32 v14, v14, v90, v89
	v_perm_b32 v2, v6, v2, v91
	v_perm_b32 v10, v14, v10, v91
	v_lshl_or_b32 v66, v10, 16, v2
	v_fmamk_f32 v18, v18, 0x44800000, v88
	v_fmamk_f32 v22, v22, 0x44800000, v88
	v_fmamk_f32 v26, v26, 0x44800000, v88
	v_fmamk_f32 v30, v30, 0x44800000, v88
	v_med3_f32 v18, v18, v90, v89
	v_med3_f32 v22, v22, v90, v89
	v_med3_f32 v26, v26, v90, v89
	v_med3_f32 v30, v30, v90, v89
	v_perm_b32 v18, v22, v18, v91
	v_perm_b32 v26, v30, v26, v91
	v_lshl_or_b32 v67, v26, 16, v18
	v_fmamk_f32 v34, v34, 0x44800000, v88
	v_fmamk_f32 v38, v38, 0x44800000, v88
	v_fmamk_f32 v42, v42, 0x44800000, v88
	v_fmamk_f32 v46, v46, 0x44800000, v88
	v_med3_f32 v34, v34, v90, v89
	v_med3_f32 v38, v38, v90, v89
	v_med3_f32 v42, v42, v90, v89
	v_med3_f32 v46, v46, v90, v89
	v_perm_b32 v34, v38, v34, v91
	v_perm_b32 v42, v46, v42, v91
	v_lshl_or_b32 v68, v42, 16, v34
	v_fmamk_f32 v50, v50, 0x44800000, v88
	v_fmamk_f32 v54, v54, 0x44800000, v88
	v_fmamk_f32 v58, v58, 0x44800000, v88
	v_fmamk_f32 v62, v62, 0x44800000, v88
	v_med3_f32 v50, v50, v90, v89
	v_med3_f32 v54, v54, v90, v89
	v_med3_f32 v58, v58, v90, v89
	v_med3_f32 v62, v62, v90, v89
	v_perm_b32 v50, v54, v50, v91
	v_perm_b32 v58, v62, v58, v91
	v_lshl_or_b32 v69, v58, 16, v50
	ds_write_b128 v72, v[66:69]
	v_fmamk_f32 v3, v3, 0x44800000, v88
	v_fmamk_f32 v7, v7, 0x44800000, v88
	v_fmamk_f32 v11, v11, 0x44800000, v88
	v_fmamk_f32 v15, v15, 0x44800000, v88
	v_med3_f32 v3, v3, v90, v89
	v_med3_f32 v7, v7, v90, v89
	v_med3_f32 v11, v11, v90, v89
	v_med3_f32 v15, v15, v90, v89
	v_perm_b32 v3, v7, v3, v91
	v_perm_b32 v11, v15, v11, v91
	v_lshl_or_b32 v66, v11, 16, v3
	v_fmamk_f32 v19, v19, 0x44800000, v88
	v_fmamk_f32 v23, v23, 0x44800000, v88
	v_fmamk_f32 v27, v27, 0x44800000, v88
	v_fmamk_f32 v31, v31, 0x44800000, v88
	v_med3_f32 v19, v19, v90, v89
	v_med3_f32 v23, v23, v90, v89
	v_med3_f32 v27, v27, v90, v89
	v_med3_f32 v31, v31, v90, v89
	v_perm_b32 v19, v23, v19, v91
	v_perm_b32 v27, v31, v27, v91
	v_lshl_or_b32 v67, v27, 16, v19
	v_fmamk_f32 v35, v35, 0x44800000, v88
	v_fmamk_f32 v39, v39, 0x44800000, v88
	v_fmamk_f32 v43, v43, 0x44800000, v88
	v_fmamk_f32 v47, v47, 0x44800000, v88
	v_med3_f32 v35, v35, v90, v89
	v_med3_f32 v39, v39, v90, v89
	v_med3_f32 v43, v43, v90, v89
	v_med3_f32 v47, v47, v90, v89
	v_perm_b32 v35, v39, v35, v91
	v_perm_b32 v43, v47, v43, v91
	v_lshl_or_b32 v68, v43, 16, v35
	v_fmamk_f32 v51, v51, 0x44800000, v88
	v_fmamk_f32 v55, v55, 0x44800000, v88
	v_fmamk_f32 v59, v59, 0x44800000, v88
	v_fmamk_f32 v63, v63, 0x44800000, v88
	v_med3_f32 v51, v51, v90, v89
	v_med3_f32 v55, v55, v90, v89
	v_med3_f32 v59, v59, v90, v89
	v_med3_f32 v63, v63, v90, v89
	v_perm_b32 v51, v55, v51, v91
	v_perm_b32 v59, v63, v59, v91
	v_lshl_or_b32 v69, v59, 16, v51
	ds_write_b128 v72, v[66:69] offset:528
	v_fmamk_f32 v4, v4, 0x44800000, v88
	v_fmamk_f32 v8, v8, 0x44800000, v88
	v_fmamk_f32 v12, v12, 0x44800000, v88
	v_fmamk_f32 v16, v16, 0x44800000, v88
	v_med3_f32 v4, v4, v90, v89
	v_med3_f32 v8, v8, v90, v89
	v_med3_f32 v12, v12, v90, v89
	v_med3_f32 v16, v16, v90, v89
	v_perm_b32 v4, v8, v4, v91
	v_perm_b32 v12, v16, v12, v91
	v_lshl_or_b32 v66, v12, 16, v4
	v_fmamk_f32 v20, v20, 0x44800000, v88
	v_fmamk_f32 v24, v24, 0x44800000, v88
	v_fmamk_f32 v28, v28, 0x44800000, v88
	v_fmamk_f32 v32, v32, 0x44800000, v88
	v_med3_f32 v20, v20, v90, v89
	v_med3_f32 v24, v24, v90, v89
	v_med3_f32 v28, v28, v90, v89
	v_med3_f32 v32, v32, v90, v89
	v_perm_b32 v20, v24, v20, v91
	v_perm_b32 v28, v32, v28, v91
	v_lshl_or_b32 v67, v28, 16, v20
	v_fmamk_f32 v36, v36, 0x44800000, v88
	v_fmamk_f32 v40, v40, 0x44800000, v88
	v_fmamk_f32 v44, v44, 0x44800000, v88
	v_fmamk_f32 v48, v48, 0x44800000, v88
	v_med3_f32 v36, v36, v90, v89
	v_med3_f32 v40, v40, v90, v89
	v_med3_f32 v44, v44, v90, v89
	v_med3_f32 v48, v48, v90, v89
	v_perm_b32 v36, v40, v36, v91
	v_perm_b32 v44, v48, v44, v91
	v_lshl_or_b32 v68, v44, 16, v36
	v_fmamk_f32 v52, v52, 0x44800000, v88
	v_fmamk_f32 v56, v56, 0x44800000, v88
	v_fmamk_f32 v60, v60, 0x44800000, v88
	v_fmamk_f32 v64, v64, 0x44800000, v88
	v_med3_f32 v52, v52, v90, v89
	v_med3_f32 v56, v56, v90, v89
	v_med3_f32 v60, v60, v90, v89
	v_med3_f32 v64, v64, v90, v89
	v_perm_b32 v52, v56, v52, v91
	v_perm_b32 v60, v64, v60, v91
	v_lshl_or_b32 v69, v60, 16, v52
	ds_write_b128 v72, v[66:69] offset:1056
	v_fmamk_f32 v5, v5, 0x44800000, v88
	v_fmamk_f32 v9, v9, 0x44800000, v88
	v_fmamk_f32 v13, v13, 0x44800000, v88
	v_fmamk_f32 v17, v17, 0x44800000, v88
	v_med3_f32 v5, v5, v90, v89
	v_med3_f32 v9, v9, v90, v89
	v_med3_f32 v13, v13, v90, v89
	v_med3_f32 v17, v17, v90, v89
	v_perm_b32 v5, v9, v5, v91
	v_perm_b32 v13, v17, v13, v91
	v_lshl_or_b32 v66, v13, 16, v5
	v_fmamk_f32 v21, v21, 0x44800000, v88
	v_fmamk_f32 v25, v25, 0x44800000, v88
	v_fmamk_f32 v29, v29, 0x44800000, v88
	v_fmamk_f32 v33, v33, 0x44800000, v88
	v_med3_f32 v21, v21, v90, v89
	v_med3_f32 v25, v25, v90, v89
	v_med3_f32 v29, v29, v90, v89
	v_med3_f32 v33, v33, v90, v89
	v_perm_b32 v21, v25, v21, v91
	v_perm_b32 v29, v33, v29, v91
	v_lshl_or_b32 v67, v29, 16, v21
	v_fmamk_f32 v37, v37, 0x44800000, v88
	v_fmamk_f32 v41, v41, 0x44800000, v88
	v_fmamk_f32 v45, v45, 0x44800000, v88
	v_fmamk_f32 v49, v49, 0x44800000, v88
	v_med3_f32 v37, v37, v90, v89
	v_med3_f32 v41, v41, v90, v89
	v_med3_f32 v45, v45, v90, v89
	v_med3_f32 v49, v49, v90, v89
	v_perm_b32 v37, v41, v37, v91
	v_perm_b32 v45, v49, v45, v91
	v_lshl_or_b32 v68, v45, 16, v37
	v_fmamk_f32 v53, v53, 0x44800000, v88
	v_fmamk_f32 v57, v57, 0x44800000, v88
	v_fmamk_f32 v61, v61, 0x44800000, v88
	v_fmamk_f32 v65, v65, 0x44800000, v88
	v_med3_f32 v53, v53, v90, v89
	v_med3_f32 v57, v57, v90, v89
	v_med3_f32 v61, v61, v90, v89
	v_med3_f32 v65, v65, v90, v89
	v_perm_b32 v53, v57, v53, v91
	v_perm_b32 v61, v65, v61, v91
	v_lshl_or_b32 v69, v61, 16, v53
	ds_write_b128 v72, v[66:69] offset:1584
	s_mov_b64 s[28:29], 0

.LBB0_538:
	s_mov_b32 s19, s20
	s_mov_b32 s10, s84
	s_mov_b32 s78, s21
	s_mov_b32 s69, s13
	s_mov_b32 s12, s18
	s_mov_b32 s68, s11
	s_mov_b64 s[80:81], s[82:83]
	s_mov_b64 s[30:31], -1
	s_mov_b64 s[2:3], 0
	s_cmp_lt_i32 s20, 2
	s_mov_b64 s[28:29], 0
	s_cbranch_scc1 .LBB0_545
	s_cmp_eq_u32 s19, 2
	s_mov_b64 s[28:29], -1
	s_cbranch_scc0 .LBB0_541
	s_waitcnt vmcnt(0)
	v_mov_b32_e32 v77, 0x4b400000
	v_mov_b32_e32 v79, 0x4b40007f
	v_mov_b32_e32 v82, 0x4b3fff81
	v_mov_b32_e32 v83, 0xc0c0400
	v_add_u32_e32 v74, v199, v198
	v_fmamk_f32 v2, v2, 0x44800000, v77
	v_fmamk_f32 v6, v6, 0x44800000, v77
	v_fmamk_f32 v10, v10, 0x44800000, v77
	v_fmamk_f32 v14, v14, 0x44800000, v77
	v_med3_f32 v2, v2, v82, v79
	v_med3_f32 v6, v6, v82, v79
	v_med3_f32 v10, v10, v82, v79
	v_med3_f32 v14, v14, v82, v79
	v_perm_b32 v2, v6, v2, v83
	v_perm_b32 v10, v14, v10, v83
	v_lshl_or_b32 v66, v10, 16, v2
	v_fmamk_f32 v18, v18, 0x44800000, v77
	v_fmamk_f32 v22, v22, 0x44800000, v77
	v_fmamk_f32 v26, v26, 0x44800000, v77
	v_fmamk_f32 v30, v30, 0x44800000, v77
	v_med3_f32 v18, v18, v82, v79
	v_med3_f32 v22, v22, v82, v79
	v_med3_f32 v26, v26, v82, v79
	v_med3_f32 v30, v30, v82, v79
	v_perm_b32 v18, v22, v18, v83
	v_perm_b32 v26, v30, v26, v83
	v_lshl_or_b32 v67, v26, 16, v18
	v_fmamk_f32 v34, v34, 0x44800000, v77
	v_fmamk_f32 v38, v38, 0x44800000, v77
	v_fmamk_f32 v42, v42, 0x44800000, v77
	v_fmamk_f32 v46, v46, 0x44800000, v77
	v_med3_f32 v34, v34, v82, v79
	v_med3_f32 v38, v38, v82, v79
	v_med3_f32 v42, v42, v82, v79
	v_med3_f32 v46, v46, v82, v79
	v_perm_b32 v34, v38, v34, v83
	v_perm_b32 v42, v46, v42, v83
	v_lshl_or_b32 v68, v42, 16, v34
	v_fmamk_f32 v50, v50, 0x44800000, v77
	v_fmamk_f32 v54, v54, 0x44800000, v77
	v_fmamk_f32 v58, v58, 0x44800000, v77
	v_fmamk_f32 v62, v62, 0x44800000, v77
	v_med3_f32 v50, v50, v82, v79
	v_med3_f32 v54, v54, v82, v79
	v_med3_f32 v58, v58, v82, v79
	v_med3_f32 v62, v62, v82, v79
	v_perm_b32 v50, v54, v50, v83
	v_perm_b32 v58, v62, v58, v83
	v_lshl_or_b32 v69, v58, 16, v50
	ds_write_b128 v74, v[66:69]
	v_fmamk_f32 v3, v3, 0x44800000, v77
	v_fmamk_f32 v7, v7, 0x44800000, v77
	v_fmamk_f32 v11, v11, 0x44800000, v77
	v_fmamk_f32 v15, v15, 0x44800000, v77
	v_med3_f32 v3, v3, v82, v79
	v_med3_f32 v7, v7, v82, v79
	v_med3_f32 v11, v11, v82, v79
	v_med3_f32 v15, v15, v82, v79
	v_perm_b32 v3, v7, v3, v83
	v_perm_b32 v11, v15, v11, v83
	v_lshl_or_b32 v66, v11, 16, v3
	v_fmamk_f32 v19, v19, 0x44800000, v77
	v_fmamk_f32 v23, v23, 0x44800000, v77
	v_fmamk_f32 v27, v27, 0x44800000, v77
	v_fmamk_f32 v31, v31, 0x44800000, v77
	v_med3_f32 v19, v19, v82, v79
	v_med3_f32 v23, v23, v82, v79
	v_med3_f32 v27, v27, v82, v79
	v_med3_f32 v31, v31, v82, v79
	v_perm_b32 v19, v23, v19, v83
	v_perm_b32 v27, v31, v27, v83
	v_lshl_or_b32 v67, v27, 16, v19
	v_fmamk_f32 v35, v35, 0x44800000, v77
	v_fmamk_f32 v39, v39, 0x44800000, v77
	v_fmamk_f32 v43, v43, 0x44800000, v77
	v_fmamk_f32 v47, v47, 0x44800000, v77
	v_med3_f32 v35, v35, v82, v79
	v_med3_f32 v39, v39, v82, v79
	v_med3_f32 v43, v43, v82, v79
	v_med3_f32 v47, v47, v82, v79
	v_perm_b32 v35, v39, v35, v83
	v_perm_b32 v43, v47, v43, v83
	v_lshl_or_b32 v68, v43, 16, v35
	v_fmamk_f32 v51, v51, 0x44800000, v77
	v_fmamk_f32 v55, v55, 0x44800000, v77
	v_fmamk_f32 v59, v59, 0x44800000, v77
	v_fmamk_f32 v63, v63, 0x44800000, v77
	v_med3_f32 v51, v51, v82, v79
	v_med3_f32 v55, v55, v82, v79
	v_med3_f32 v59, v59, v82, v79
	v_med3_f32 v63, v63, v82, v79
	v_perm_b32 v51, v55, v51, v83
	v_perm_b32 v59, v63, v59, v83
	v_lshl_or_b32 v69, v59, 16, v51
	ds_write_b128 v74, v[66:69] offset:528
	v_fmamk_f32 v4, v4, 0x44800000, v77
	v_fmamk_f32 v8, v8, 0x44800000, v77
	v_fmamk_f32 v12, v12, 0x44800000, v77
	v_fmamk_f32 v16, v16, 0x44800000, v77
	v_med3_f32 v4, v4, v82, v79
	v_med3_f32 v8, v8, v82, v79
	v_med3_f32 v12, v12, v82, v79
	v_med3_f32 v16, v16, v82, v79
	v_perm_b32 v4, v8, v4, v83
	v_perm_b32 v12, v16, v12, v83
	v_lshl_or_b32 v66, v12, 16, v4
	v_fmamk_f32 v20, v20, 0x44800000, v77
	v_fmamk_f32 v24, v24, 0x44800000, v77
	v_fmamk_f32 v28, v28, 0x44800000, v77
	v_fmamk_f32 v32, v32, 0x44800000, v77
	v_med3_f32 v20, v20, v82, v79
	v_med3_f32 v24, v24, v82, v79
	v_med3_f32 v28, v28, v82, v79
	v_med3_f32 v32, v32, v82, v79
	v_perm_b32 v20, v24, v20, v83
	v_perm_b32 v28, v32, v28, v83
	v_lshl_or_b32 v67, v28, 16, v20
	v_fmamk_f32 v36, v36, 0x44800000, v77
	v_fmamk_f32 v40, v40, 0x44800000, v77
	v_fmamk_f32 v44, v44, 0x44800000, v77
	v_fmamk_f32 v48, v48, 0x44800000, v77
	v_med3_f32 v36, v36, v82, v79
	v_med3_f32 v40, v40, v82, v79
	v_med3_f32 v44, v44, v82, v79
	v_med3_f32 v48, v48, v82, v79
	v_perm_b32 v36, v40, v36, v83
	v_perm_b32 v44, v48, v44, v83
	v_lshl_or_b32 v68, v44, 16, v36
	v_fmamk_f32 v52, v52, 0x44800000, v77
	v_fmamk_f32 v56, v56, 0x44800000, v77
	v_fmamk_f32 v60, v60, 0x44800000, v77
	v_fmamk_f32 v64, v64, 0x44800000, v77
	v_med3_f32 v52, v52, v82, v79
	v_med3_f32 v56, v56, v82, v79
	v_med3_f32 v60, v60, v82, v79
	v_med3_f32 v64, v64, v82, v79
	v_perm_b32 v52, v56, v52, v83
	v_perm_b32 v60, v64, v60, v83
	v_lshl_or_b32 v69, v60, 16, v52
	ds_write_b128 v74, v[66:69] offset:1056
	v_fmamk_f32 v5, v5, 0x44800000, v77
	v_fmamk_f32 v9, v9, 0x44800000, v77
	v_fmamk_f32 v13, v13, 0x44800000, v77
	v_fmamk_f32 v17, v17, 0x44800000, v77
	v_med3_f32 v5, v5, v82, v79
	v_med3_f32 v9, v9, v82, v79
	v_med3_f32 v13, v13, v82, v79
	v_med3_f32 v17, v17, v82, v79
	v_perm_b32 v5, v9, v5, v83
	v_perm_b32 v13, v17, v13, v83
	v_lshl_or_b32 v66, v13, 16, v5
	v_fmamk_f32 v21, v21, 0x44800000, v77
	v_fmamk_f32 v25, v25, 0x44800000, v77
	v_fmamk_f32 v29, v29, 0x44800000, v77
	v_fmamk_f32 v33, v33, 0x44800000, v77
	v_med3_f32 v21, v21, v82, v79
	v_med3_f32 v25, v25, v82, v79
	v_med3_f32 v29, v29, v82, v79
	v_med3_f32 v33, v33, v82, v79
	v_perm_b32 v21, v25, v21, v83
	v_perm_b32 v29, v33, v29, v83
	v_lshl_or_b32 v67, v29, 16, v21
	v_fmamk_f32 v37, v37, 0x44800000, v77
	v_fmamk_f32 v41, v41, 0x44800000, v77
	v_fmamk_f32 v45, v45, 0x44800000, v77
	v_fmamk_f32 v49, v49, 0x44800000, v77
	v_med3_f32 v37, v37, v82, v79
	v_med3_f32 v41, v41, v82, v79
	v_med3_f32 v45, v45, v82, v79
	v_med3_f32 v49, v49, v82, v79
	v_perm_b32 v37, v41, v37, v83
	v_perm_b32 v45, v49, v45, v83
	v_lshl_or_b32 v68, v45, 16, v37
	v_fmamk_f32 v53, v53, 0x44800000, v77
	v_fmamk_f32 v57, v57, 0x44800000, v77
	v_fmamk_f32 v61, v61, 0x44800000, v77
	v_fmamk_f32 v65, v65, 0x44800000, v77
	v_med3_f32 v53, v53, v82, v79
	v_med3_f32 v57, v57, v82, v79
	v_med3_f32 v61, v61, v82, v79
	v_med3_f32 v65, v65, v82, v79
	v_perm_b32 v53, v57, v53, v83
	v_perm_b32 v61, v65, v61, v83
	v_lshl_or_b32 v69, v61, 16, v53
	ds_write_b128 v74, v[66:69] offset:1584
	s_mov_b64 s[28:29], 0

.LBB0_779:
	v_readlane_b32 s36, v254, 38
	s_mov_b32 s19, s20
	s_mov_b32 s10, s82
	s_mov_b32 s74, s21
	s_mov_b32 s67, s13
	s_mov_b32 s12, s18
	s_mov_b32 s66, s11
	s_mov_b64 s[78:79], s[80:81]
	s_mov_b64 s[30:31], -1
	s_mov_b64 s[2:3], 0
	s_cmp_lt_i32 s20, 2
	s_mov_b64 s[28:29], 0
	v_readlane_b32 s50, v254, 52
	v_readlane_b32 s51, v254, 53
	v_readlane_b32 s37, v254, 39
	v_readlane_b32 s38, v254, 40
	v_readlane_b32 s39, v254, 41
	v_readlane_b32 s40, v254, 42
	v_readlane_b32 s41, v254, 43
	v_readlane_b32 s42, v254, 44
	v_readlane_b32 s43, v254, 45
	v_readlane_b32 s44, v254, 46
	v_readlane_b32 s45, v254, 47
	v_readlane_b32 s46, v254, 48
	v_readlane_b32 s47, v254, 49
	v_readlane_b32 s48, v254, 50
	v_readlane_b32 s49, v254, 51
	s_cbranch_scc1 .LBB0_786
	s_cmp_eq_u32 s19, 2
	s_mov_b64 s[28:29], -1
	s_cbranch_scc0 .LBB0_782
	s_waitcnt vmcnt(0)
	v_mov_b32_e32 v73, 0x4b400000
	v_mov_b32_e32 v74, 0x4b40007f
	v_mov_b32_e32 v75, 0x4b3fff81
	v_mov_b32_e32 v76, 0xc0c0400
	v_add_u32_e32 v70, v199, v198
	v_fmamk_f32 v2, v2, 0x44800000, v73
	v_fmamk_f32 v6, v6, 0x44800000, v73
	v_fmamk_f32 v10, v10, 0x44800000, v73
	v_fmamk_f32 v14, v14, 0x44800000, v73
	v_med3_f32 v2, v2, v75, v74
	v_med3_f32 v6, v6, v75, v74
	v_med3_f32 v10, v10, v75, v74
	v_med3_f32 v14, v14, v75, v74
	v_perm_b32 v2, v6, v2, v76
	v_perm_b32 v10, v14, v10, v76
	v_lshl_or_b32 v66, v10, 16, v2
	v_fmamk_f32 v18, v18, 0x44800000, v73
	v_fmamk_f32 v22, v22, 0x44800000, v73
	v_fmamk_f32 v26, v26, 0x44800000, v73
	v_fmamk_f32 v30, v30, 0x44800000, v73
	v_med3_f32 v18, v18, v75, v74
	v_med3_f32 v22, v22, v75, v74
	v_med3_f32 v26, v26, v75, v74
	v_med3_f32 v30, v30, v75, v74
	v_perm_b32 v18, v22, v18, v76
	v_perm_b32 v26, v30, v26, v76
	v_lshl_or_b32 v67, v26, 16, v18
	v_fmamk_f32 v34, v34, 0x44800000, v73
	v_fmamk_f32 v38, v38, 0x44800000, v73
	v_fmamk_f32 v42, v42, 0x44800000, v73
	v_fmamk_f32 v46, v46, 0x44800000, v73
	v_med3_f32 v34, v34, v75, v74
	v_med3_f32 v38, v38, v75, v74
	v_med3_f32 v42, v42, v75, v74
	v_med3_f32 v46, v46, v75, v74
	v_perm_b32 v34, v38, v34, v76
	v_perm_b32 v42, v46, v42, v76
	v_lshl_or_b32 v68, v42, 16, v34
	v_fmamk_f32 v50, v50, 0x44800000, v73
	v_fmamk_f32 v54, v54, 0x44800000, v73
	v_fmamk_f32 v58, v58, 0x44800000, v73
	v_fmamk_f32 v62, v62, 0x44800000, v73
	v_med3_f32 v50, v50, v75, v74
	v_med3_f32 v54, v54, v75, v74
	v_med3_f32 v58, v58, v75, v74
	v_med3_f32 v62, v62, v75, v74
	v_perm_b32 v50, v54, v50, v76
	v_perm_b32 v58, v62, v58, v76
	v_lshl_or_b32 v69, v58, 16, v50
	ds_write_b128 v70, v[66:69]
	v_fmamk_f32 v3, v3, 0x44800000, v73
	v_fmamk_f32 v7, v7, 0x44800000, v73
	v_fmamk_f32 v11, v11, 0x44800000, v73
	v_fmamk_f32 v15, v15, 0x44800000, v73
	v_med3_f32 v3, v3, v75, v74
	v_med3_f32 v7, v7, v75, v74
	v_med3_f32 v11, v11, v75, v74
	v_med3_f32 v15, v15, v75, v74
	v_perm_b32 v3, v7, v3, v76
	v_perm_b32 v11, v15, v11, v76
	v_lshl_or_b32 v66, v11, 16, v3
	v_fmamk_f32 v19, v19, 0x44800000, v73
	v_fmamk_f32 v23, v23, 0x44800000, v73
	v_fmamk_f32 v27, v27, 0x44800000, v73
	v_fmamk_f32 v31, v31, 0x44800000, v73
	v_med3_f32 v19, v19, v75, v74
	v_med3_f32 v23, v23, v75, v74
	v_med3_f32 v27, v27, v75, v74
	v_med3_f32 v31, v31, v75, v74
	v_perm_b32 v19, v23, v19, v76
	v_perm_b32 v27, v31, v27, v76
	v_lshl_or_b32 v67, v27, 16, v19
	v_fmamk_f32 v35, v35, 0x44800000, v73
	v_fmamk_f32 v39, v39, 0x44800000, v73
	v_fmamk_f32 v43, v43, 0x44800000, v73
	v_fmamk_f32 v47, v47, 0x44800000, v73
	v_med3_f32 v35, v35, v75, v74
	v_med3_f32 v39, v39, v75, v74
	v_med3_f32 v43, v43, v75, v74
	v_med3_f32 v47, v47, v75, v74
	v_perm_b32 v35, v39, v35, v76
	v_perm_b32 v43, v47, v43, v76
	v_lshl_or_b32 v68, v43, 16, v35
	v_fmamk_f32 v51, v51, 0x44800000, v73
	v_fmamk_f32 v55, v55, 0x44800000, v73
	v_fmamk_f32 v59, v59, 0x44800000, v73
	v_fmamk_f32 v63, v63, 0x44800000, v73
	v_med3_f32 v51, v51, v75, v74
	v_med3_f32 v55, v55, v75, v74
	v_med3_f32 v59, v59, v75, v74
	v_med3_f32 v63, v63, v75, v74
	v_perm_b32 v51, v55, v51, v76
	v_perm_b32 v59, v63, v59, v76
	v_lshl_or_b32 v69, v59, 16, v51
	ds_write_b128 v70, v[66:69] offset:528
	v_fmamk_f32 v4, v4, 0x44800000, v73
	v_fmamk_f32 v8, v8, 0x44800000, v73
	v_fmamk_f32 v12, v12, 0x44800000, v73
	v_fmamk_f32 v16, v16, 0x44800000, v73
	v_med3_f32 v4, v4, v75, v74
	v_med3_f32 v8, v8, v75, v74
	v_med3_f32 v12, v12, v75, v74
	v_med3_f32 v16, v16, v75, v74
	v_perm_b32 v4, v8, v4, v76
	v_perm_b32 v12, v16, v12, v76
	v_lshl_or_b32 v66, v12, 16, v4
	v_fmamk_f32 v20, v20, 0x44800000, v73
	v_fmamk_f32 v24, v24, 0x44800000, v73
	v_fmamk_f32 v28, v28, 0x44800000, v73
	v_fmamk_f32 v32, v32, 0x44800000, v73
	v_med3_f32 v20, v20, v75, v74
	v_med3_f32 v24, v24, v75, v74
	v_med3_f32 v28, v28, v75, v74
	v_med3_f32 v32, v32, v75, v74
	v_perm_b32 v20, v24, v20, v76
	v_perm_b32 v28, v32, v28, v76
	v_lshl_or_b32 v67, v28, 16, v20
	v_fmamk_f32 v36, v36, 0x44800000, v73
	v_fmamk_f32 v40, v40, 0x44800000, v73
	v_fmamk_f32 v44, v44, 0x44800000, v73
	v_fmamk_f32 v48, v48, 0x44800000, v73
	v_med3_f32 v36, v36, v75, v74
	v_med3_f32 v40, v40, v75, v74
	v_med3_f32 v44, v44, v75, v74
	v_med3_f32 v48, v48, v75, v74
	v_perm_b32 v36, v40, v36, v76
	v_perm_b32 v44, v48, v44, v76
	v_lshl_or_b32 v68, v44, 16, v36
	v_fmamk_f32 v52, v52, 0x44800000, v73
	v_fmamk_f32 v56, v56, 0x44800000, v73
	v_fmamk_f32 v60, v60, 0x44800000, v73
	v_fmamk_f32 v64, v64, 0x44800000, v73
	v_med3_f32 v52, v52, v75, v74
	v_med3_f32 v56, v56, v75, v74
	v_med3_f32 v60, v60, v75, v74
	v_med3_f32 v64, v64, v75, v74
	v_perm_b32 v52, v56, v52, v76
	v_perm_b32 v60, v64, v60, v76
	v_lshl_or_b32 v69, v60, 16, v52
	ds_write_b128 v70, v[66:69] offset:1056
	v_fmamk_f32 v5, v5, 0x44800000, v73
	v_fmamk_f32 v9, v9, 0x44800000, v73
	v_fmamk_f32 v13, v13, 0x44800000, v73
	v_fmamk_f32 v17, v17, 0x44800000, v73
	v_med3_f32 v5, v5, v75, v74
	v_med3_f32 v9, v9, v75, v74
	v_med3_f32 v13, v13, v75, v74
	v_med3_f32 v17, v17, v75, v74
	v_perm_b32 v5, v9, v5, v76
	v_perm_b32 v13, v17, v13, v76
	v_lshl_or_b32 v66, v13, 16, v5
	v_fmamk_f32 v21, v21, 0x44800000, v73
	v_fmamk_f32 v25, v25, 0x44800000, v73
	v_fmamk_f32 v29, v29, 0x44800000, v73
	v_fmamk_f32 v33, v33, 0x44800000, v73
	v_med3_f32 v21, v21, v75, v74
	v_med3_f32 v25, v25, v75, v74
	v_med3_f32 v29, v29, v75, v74
	v_med3_f32 v33, v33, v75, v74
	v_perm_b32 v21, v25, v21, v76
	v_perm_b32 v29, v33, v29, v76
	v_lshl_or_b32 v67, v29, 16, v21
	v_fmamk_f32 v37, v37, 0x44800000, v73
	v_fmamk_f32 v41, v41, 0x44800000, v73
	v_fmamk_f32 v45, v45, 0x44800000, v73
	v_fmamk_f32 v49, v49, 0x44800000, v73
	v_med3_f32 v37, v37, v75, v74
	v_med3_f32 v41, v41, v75, v74
	v_med3_f32 v45, v45, v75, v74
	v_med3_f32 v49, v49, v75, v74
	v_perm_b32 v37, v41, v37, v76
	v_perm_b32 v45, v49, v45, v76
	v_lshl_or_b32 v68, v45, 16, v37
	v_fmamk_f32 v53, v53, 0x44800000, v73
	v_fmamk_f32 v57, v57, 0x44800000, v73
	v_fmamk_f32 v61, v61, 0x44800000, v73
	v_fmamk_f32 v65, v65, 0x44800000, v73
	v_med3_f32 v53, v53, v75, v74
	v_med3_f32 v57, v57, v75, v74
	v_med3_f32 v61, v61, v75, v74
	v_med3_f32 v65, v65, v75, v74
	v_perm_b32 v53, v57, v53, v76
	v_perm_b32 v61, v65, v61, v76
	v_lshl_or_b32 v69, v61, 16, v53
	ds_write_b128 v70, v[66:69] offset:1584
	s_mov_b64 s[28:29], 0

.LBB0_1073:
	v_readlane_b32 s36, v254, 38
	s_mov_b32 s22, s21
	s_mov_b32 s13, s82
	s_mov_b32 s74, s23
	s_mov_b32 s11, s19
	s_mov_b32 s12, s20
	s_mov_b32 s10, s18
	s_mov_b64 s[78:79], s[80:81]
	s_mov_b64 s[30:31], -1
	s_mov_b64 s[2:3], 0
	s_cmp_lt_i32 s21, 2
	s_mov_b64 s[28:29], 0
	v_readlane_b32 s50, v254, 52
	v_readlane_b32 s51, v254, 53
	v_readlane_b32 s37, v254, 39
	v_readlane_b32 s38, v254, 40
	v_readlane_b32 s39, v254, 41
	v_readlane_b32 s40, v254, 42
	v_readlane_b32 s41, v254, 43
	v_readlane_b32 s42, v254, 44
	v_readlane_b32 s43, v254, 45
	v_readlane_b32 s44, v254, 46
	v_readlane_b32 s45, v254, 47
	v_readlane_b32 s46, v254, 48
	v_readlane_b32 s47, v254, 49
	v_readlane_b32 s48, v254, 50
	v_readlane_b32 s49, v254, 51
	s_cbranch_scc1 .LBB0_1080
	s_cmp_eq_u32 s22, 2
	s_mov_b64 s[28:29], -1
	s_cbranch_scc0 .LBB0_1076
	s_waitcnt vmcnt(0)
	v_mov_b32_e32 v73, 0x4b400000
	v_mov_b32_e32 v74, 0x4b40007f
	v_mov_b32_e32 v75, 0x4b3fff81
	v_mov_b32_e32 v76, 0xc0c0400
	v_add_u32_e32 v70, v199, v198
	v_fmamk_f32 v2, v2, 0x44800000, v73
	v_fmamk_f32 v6, v6, 0x44800000, v73
	v_fmamk_f32 v10, v10, 0x44800000, v73
	v_fmamk_f32 v14, v14, 0x44800000, v73
	v_med3_f32 v2, v2, v75, v74
	v_med3_f32 v6, v6, v75, v74
	v_med3_f32 v10, v10, v75, v74
	v_med3_f32 v14, v14, v75, v74
	v_perm_b32 v2, v6, v2, v76
	v_perm_b32 v10, v14, v10, v76
	v_lshl_or_b32 v66, v10, 16, v2
	v_fmamk_f32 v18, v18, 0x44800000, v73
	v_fmamk_f32 v22, v22, 0x44800000, v73
	v_fmamk_f32 v26, v26, 0x44800000, v73
	v_fmamk_f32 v30, v30, 0x44800000, v73
	v_med3_f32 v18, v18, v75, v74
	v_med3_f32 v22, v22, v75, v74
	v_med3_f32 v26, v26, v75, v74
	v_med3_f32 v30, v30, v75, v74
	v_perm_b32 v18, v22, v18, v76
	v_perm_b32 v26, v30, v26, v76
	v_lshl_or_b32 v67, v26, 16, v18
	v_fmamk_f32 v34, v34, 0x44800000, v73
	v_fmamk_f32 v38, v38, 0x44800000, v73
	v_fmamk_f32 v42, v42, 0x44800000, v73
	v_fmamk_f32 v46, v46, 0x44800000, v73
	v_med3_f32 v34, v34, v75, v74
	v_med3_f32 v38, v38, v75, v74
	v_med3_f32 v42, v42, v75, v74
	v_med3_f32 v46, v46, v75, v74
	v_perm_b32 v34, v38, v34, v76
	v_perm_b32 v42, v46, v42, v76
	v_lshl_or_b32 v68, v42, 16, v34
	v_fmamk_f32 v50, v50, 0x44800000, v73
	v_fmamk_f32 v54, v54, 0x44800000, v73
	v_fmamk_f32 v58, v58, 0x44800000, v73
	v_fmamk_f32 v62, v62, 0x44800000, v73
	v_med3_f32 v50, v50, v75, v74
	v_med3_f32 v54, v54, v75, v74
	v_med3_f32 v58, v58, v75, v74
	v_med3_f32 v62, v62, v75, v74
	v_perm_b32 v50, v54, v50, v76
	v_perm_b32 v58, v62, v58, v76
	v_lshl_or_b32 v69, v58, 16, v50
	ds_write_b128 v70, v[66:69]
	v_fmamk_f32 v3, v3, 0x44800000, v73
	v_fmamk_f32 v7, v7, 0x44800000, v73
	v_fmamk_f32 v11, v11, 0x44800000, v73
	v_fmamk_f32 v15, v15, 0x44800000, v73
	v_med3_f32 v3, v3, v75, v74
	v_med3_f32 v7, v7, v75, v74
	v_med3_f32 v11, v11, v75, v74
	v_med3_f32 v15, v15, v75, v74
	v_perm_b32 v3, v7, v3, v76
	v_perm_b32 v11, v15, v11, v76
	v_lshl_or_b32 v66, v11, 16, v3
	v_fmamk_f32 v19, v19, 0x44800000, v73
	v_fmamk_f32 v23, v23, 0x44800000, v73
	v_fmamk_f32 v27, v27, 0x44800000, v73
	v_fmamk_f32 v31, v31, 0x44800000, v73
	v_med3_f32 v19, v19, v75, v74
	v_med3_f32 v23, v23, v75, v74
	v_med3_f32 v27, v27, v75, v74
	v_med3_f32 v31, v31, v75, v74
	v_perm_b32 v19, v23, v19, v76
	v_perm_b32 v27, v31, v27, v76
	v_lshl_or_b32 v67, v27, 16, v19
	v_fmamk_f32 v35, v35, 0x44800000, v73
	v_fmamk_f32 v39, v39, 0x44800000, v73
	v_fmamk_f32 v43, v43, 0x44800000, v73
	v_fmamk_f32 v47, v47, 0x44800000, v73
	v_med3_f32 v35, v35, v75, v74
	v_med3_f32 v39, v39, v75, v74
	v_med3_f32 v43, v43, v75, v74
	v_med3_f32 v47, v47, v75, v74
	v_perm_b32 v35, v39, v35, v76
	v_perm_b32 v43, v47, v43, v76
	v_lshl_or_b32 v68, v43, 16, v35
	v_fmamk_f32 v51, v51, 0x44800000, v73
	v_fmamk_f32 v55, v55, 0x44800000, v73
	v_fmamk_f32 v59, v59, 0x44800000, v73
	v_fmamk_f32 v63, v63, 0x44800000, v73
	v_med3_f32 v51, v51, v75, v74
	v_med3_f32 v55, v55, v75, v74
	v_med3_f32 v59, v59, v75, v74
	v_med3_f32 v63, v63, v75, v74
	v_perm_b32 v51, v55, v51, v76
	v_perm_b32 v59, v63, v59, v76
	v_lshl_or_b32 v69, v59, 16, v51
	ds_write_b128 v70, v[66:69] offset:528
	v_fmamk_f32 v4, v4, 0x44800000, v73
	v_fmamk_f32 v8, v8, 0x44800000, v73
	v_fmamk_f32 v12, v12, 0x44800000, v73
	v_fmamk_f32 v16, v16, 0x44800000, v73
	v_med3_f32 v4, v4, v75, v74
	v_med3_f32 v8, v8, v75, v74
	v_med3_f32 v12, v12, v75, v74
	v_med3_f32 v16, v16, v75, v74
	v_perm_b32 v4, v8, v4, v76
	v_perm_b32 v12, v16, v12, v76
	v_lshl_or_b32 v66, v12, 16, v4
	v_fmamk_f32 v20, v20, 0x44800000, v73
	v_fmamk_f32 v24, v24, 0x44800000, v73
	v_fmamk_f32 v28, v28, 0x44800000, v73
	v_fmamk_f32 v32, v32, 0x44800000, v73
	v_med3_f32 v20, v20, v75, v74
	v_med3_f32 v24, v24, v75, v74
	v_med3_f32 v28, v28, v75, v74
	v_med3_f32 v32, v32, v75, v74
	v_perm_b32 v20, v24, v20, v76
	v_perm_b32 v28, v32, v28, v76
	v_lshl_or_b32 v67, v28, 16, v20
	v_fmamk_f32 v36, v36, 0x44800000, v73
	v_fmamk_f32 v40, v40, 0x44800000, v73
	v_fmamk_f32 v44, v44, 0x44800000, v73
	v_fmamk_f32 v48, v48, 0x44800000, v73
	v_med3_f32 v36, v36, v75, v74
	v_med3_f32 v40, v40, v75, v74
	v_med3_f32 v44, v44, v75, v74
	v_med3_f32 v48, v48, v75, v74
	v_perm_b32 v36, v40, v36, v76
	v_perm_b32 v44, v48, v44, v76
	v_lshl_or_b32 v68, v44, 16, v36
	v_fmamk_f32 v52, v52, 0x44800000, v73
	v_fmamk_f32 v56, v56, 0x44800000, v73
	v_fmamk_f32 v60, v60, 0x44800000, v73
	v_fmamk_f32 v64, v64, 0x44800000, v73
	v_med3_f32 v52, v52, v75, v74
	v_med3_f32 v56, v56, v75, v74
	v_med3_f32 v60, v60, v75, v74
	v_med3_f32 v64, v64, v75, v74
	v_perm_b32 v52, v56, v52, v76
	v_perm_b32 v60, v64, v60, v76
	v_lshl_or_b32 v69, v60, 16, v52
	ds_write_b128 v70, v[66:69] offset:1056
	v_fmamk_f32 v5, v5, 0x44800000, v73
	v_fmamk_f32 v9, v9, 0x44800000, v73
	v_fmamk_f32 v13, v13, 0x44800000, v73
	v_fmamk_f32 v17, v17, 0x44800000, v73
	v_med3_f32 v5, v5, v75, v74
	v_med3_f32 v9, v9, v75, v74
	v_med3_f32 v13, v13, v75, v74
	v_med3_f32 v17, v17, v75, v74
	v_perm_b32 v5, v9, v5, v76
	v_perm_b32 v13, v17, v13, v76
	v_lshl_or_b32 v66, v13, 16, v5
	v_fmamk_f32 v21, v21, 0x44800000, v73
	v_fmamk_f32 v25, v25, 0x44800000, v73
	v_fmamk_f32 v29, v29, 0x44800000, v73
	v_fmamk_f32 v33, v33, 0x44800000, v73
	v_med3_f32 v21, v21, v75, v74
	v_med3_f32 v25, v25, v75, v74
	v_med3_f32 v29, v29, v75, v74
	v_med3_f32 v33, v33, v75, v74
	v_perm_b32 v21, v25, v21, v76
	v_perm_b32 v29, v33, v29, v76
	v_lshl_or_b32 v67, v29, 16, v21
	v_fmamk_f32 v37, v37, 0x44800000, v73
	v_fmamk_f32 v41, v41, 0x44800000, v73
	v_fmamk_f32 v45, v45, 0x44800000, v73
	v_fmamk_f32 v49, v49, 0x44800000, v73
	v_med3_f32 v37, v37, v75, v74
	v_med3_f32 v41, v41, v75, v74
	v_med3_f32 v45, v45, v75, v74
	v_med3_f32 v49, v49, v75, v74
	v_perm_b32 v37, v41, v37, v76
	v_perm_b32 v45, v49, v45, v76
	v_lshl_or_b32 v68, v45, 16, v37
	v_fmamk_f32 v53, v53, 0x44800000, v73
	v_fmamk_f32 v57, v57, 0x44800000, v73
	v_fmamk_f32 v61, v61, 0x44800000, v73
	v_fmamk_f32 v65, v65, 0x44800000, v73
	v_med3_f32 v53, v53, v75, v74
	v_med3_f32 v57, v57, v75, v74
	v_med3_f32 v61, v61, v75, v74
	v_med3_f32 v65, v65, v75, v74
	v_perm_b32 v53, v57, v53, v76
	v_perm_b32 v61, v65, v61, v76
	v_lshl_or_b32 v69, v61, 16, v53
	ds_write_b128 v70, v[66:69] offset:1584
	s_mov_b64 s[28:29], 0

.LBB0_1554:
	s_mov_b32 s59, s58
	s_mov_b32 s52, s88
	s_mov_b32 s82, s60
	s_mov_b32 s27, s54
	s_mov_b32 s33, s55
	s_mov_b32 s26, s53
	s_mov_b64 s[84:85], s[86:87]
	s_mov_b64 s[30:31], -1
	s_mov_b64 s[2:3], 0
	s_cmp_lt_i32 s58, 2
	s_mov_b64 s[28:29], 0
	s_cbranch_scc1 .LBB0_1561
	s_cmp_eq_u32 s59, 2
	s_mov_b64 s[28:29], -1
	s_cbranch_scc0 .LBB0_1557
	s_waitcnt vmcnt(0)
	v_mov_b32_e32 v76, 0x4b400000
	v_mov_b32_e32 v77, 0x4b40007f
	v_mov_b32_e32 v90, 0x4b3fff81
	v_mov_b32_e32 v91, 0xc0c0400
	v_add_u32_e32 v89, v79, v78
	v_fmamk_f32 v2, v2, 0x44800000, v76
	v_fmamk_f32 v6, v6, 0x44800000, v76
	v_fmamk_f32 v10, v10, 0x44800000, v76
	v_fmamk_f32 v14, v14, 0x44800000, v76
	v_med3_f32 v2, v2, v90, v77
	v_med3_f32 v6, v6, v90, v77
	v_med3_f32 v10, v10, v90, v77
	v_med3_f32 v14, v14, v90, v77
	v_perm_b32 v2, v6, v2, v91
	v_perm_b32 v10, v14, v10, v91
	v_lshl_or_b32 v66, v10, 16, v2
	v_fmamk_f32 v18, v18, 0x44800000, v76
	v_fmamk_f32 v22, v22, 0x44800000, v76
	v_fmamk_f32 v26, v26, 0x44800000, v76
	v_fmamk_f32 v30, v30, 0x44800000, v76
	v_med3_f32 v18, v18, v90, v77
	v_med3_f32 v22, v22, v90, v77
	v_med3_f32 v26, v26, v90, v77
	v_med3_f32 v30, v30, v90, v77
	v_perm_b32 v18, v22, v18, v91
	v_perm_b32 v26, v30, v26, v91
	v_lshl_or_b32 v67, v26, 16, v18
	v_fmamk_f32 v34, v34, 0x44800000, v76
	v_fmamk_f32 v38, v38, 0x44800000, v76
	v_fmamk_f32 v42, v42, 0x44800000, v76
	v_fmamk_f32 v46, v46, 0x44800000, v76
	v_med3_f32 v34, v34, v90, v77
	v_med3_f32 v38, v38, v90, v77
	v_med3_f32 v42, v42, v90, v77
	v_med3_f32 v46, v46, v90, v77
	v_perm_b32 v34, v38, v34, v91
	v_perm_b32 v42, v46, v42, v91
	v_lshl_or_b32 v68, v42, 16, v34
	v_fmamk_f32 v50, v50, 0x44800000, v76
	v_fmamk_f32 v54, v54, 0x44800000, v76
	v_fmamk_f32 v58, v58, 0x44800000, v76
	v_fmamk_f32 v62, v62, 0x44800000, v76
	v_med3_f32 v50, v50, v90, v77
	v_med3_f32 v54, v54, v90, v77
	v_med3_f32 v58, v58, v90, v77
	v_med3_f32 v62, v62, v90, v77
	v_perm_b32 v50, v54, v50, v91
	v_perm_b32 v58, v62, v58, v91
	v_lshl_or_b32 v69, v58, 16, v50
	ds_write_b128 v89, v[66:69]
	v_fmamk_f32 v3, v3, 0x44800000, v76
	v_fmamk_f32 v7, v7, 0x44800000, v76
	v_fmamk_f32 v11, v11, 0x44800000, v76
	v_fmamk_f32 v15, v15, 0x44800000, v76
	v_med3_f32 v3, v3, v90, v77
	v_med3_f32 v7, v7, v90, v77
	v_med3_f32 v11, v11, v90, v77
	v_med3_f32 v15, v15, v90, v77
	v_perm_b32 v3, v7, v3, v91
	v_perm_b32 v11, v15, v11, v91
	v_lshl_or_b32 v66, v11, 16, v3
	v_fmamk_f32 v19, v19, 0x44800000, v76
	v_fmamk_f32 v23, v23, 0x44800000, v76
	v_fmamk_f32 v27, v27, 0x44800000, v76
	v_fmamk_f32 v31, v31, 0x44800000, v76
	v_med3_f32 v19, v19, v90, v77
	v_med3_f32 v23, v23, v90, v77
	v_med3_f32 v27, v27, v90, v77
	v_med3_f32 v31, v31, v90, v77
	v_perm_b32 v19, v23, v19, v91
	v_perm_b32 v27, v31, v27, v91
	v_lshl_or_b32 v67, v27, 16, v19
	v_fmamk_f32 v35, v35, 0x44800000, v76
	v_fmamk_f32 v39, v39, 0x44800000, v76
	v_fmamk_f32 v43, v43, 0x44800000, v76
	v_fmamk_f32 v47, v47, 0x44800000, v76
	v_med3_f32 v35, v35, v90, v77
	v_med3_f32 v39, v39, v90, v77
	v_med3_f32 v43, v43, v90, v77
	v_med3_f32 v47, v47, v90, v77
	v_perm_b32 v35, v39, v35, v91
	v_perm_b32 v43, v47, v43, v91
	v_lshl_or_b32 v68, v43, 16, v35
	v_fmamk_f32 v51, v51, 0x44800000, v76
	v_fmamk_f32 v55, v55, 0x44800000, v76
	v_fmamk_f32 v59, v59, 0x44800000, v76
	v_fmamk_f32 v63, v63, 0x44800000, v76
	v_med3_f32 v51, v51, v90, v77
	v_med3_f32 v55, v55, v90, v77
	v_med3_f32 v59, v59, v90, v77
	v_med3_f32 v63, v63, v90, v77
	v_perm_b32 v51, v55, v51, v91
	v_perm_b32 v59, v63, v59, v91
	v_lshl_or_b32 v69, v59, 16, v51
	ds_write_b128 v89, v[66:69] offset:528
	v_fmamk_f32 v4, v4, 0x44800000, v76
	v_fmamk_f32 v8, v8, 0x44800000, v76
	v_fmamk_f32 v12, v12, 0x44800000, v76
	v_fmamk_f32 v16, v16, 0x44800000, v76
	v_med3_f32 v4, v4, v90, v77
	v_med3_f32 v8, v8, v90, v77
	v_med3_f32 v12, v12, v90, v77
	v_med3_f32 v16, v16, v90, v77
	v_perm_b32 v4, v8, v4, v91
	v_perm_b32 v12, v16, v12, v91
	v_lshl_or_b32 v66, v12, 16, v4
	v_fmamk_f32 v20, v20, 0x44800000, v76
	v_fmamk_f32 v24, v24, 0x44800000, v76
	v_fmamk_f32 v28, v28, 0x44800000, v76
	v_fmamk_f32 v32, v32, 0x44800000, v76
	v_med3_f32 v20, v20, v90, v77
	v_med3_f32 v24, v24, v90, v77
	v_med3_f32 v28, v28, v90, v77
	v_med3_f32 v32, v32, v90, v77
	v_perm_b32 v20, v24, v20, v91
	v_perm_b32 v28, v32, v28, v91
	v_lshl_or_b32 v67, v28, 16, v20
	v_fmamk_f32 v36, v36, 0x44800000, v76
	v_fmamk_f32 v40, v40, 0x44800000, v76
	v_fmamk_f32 v44, v44, 0x44800000, v76
	v_fmamk_f32 v48, v48, 0x44800000, v76
	v_med3_f32 v36, v36, v90, v77
	v_med3_f32 v40, v40, v90, v77
	v_med3_f32 v44, v44, v90, v77
	v_med3_f32 v48, v48, v90, v77
	v_perm_b32 v36, v40, v36, v91
	v_perm_b32 v44, v48, v44, v91
	v_lshl_or_b32 v68, v44, 16, v36
	v_fmamk_f32 v52, v52, 0x44800000, v76
	v_fmamk_f32 v56, v56, 0x44800000, v76
	v_fmamk_f32 v60, v60, 0x44800000, v76
	v_fmamk_f32 v64, v64, 0x44800000, v76
	v_med3_f32 v52, v52, v90, v77
	v_med3_f32 v56, v56, v90, v77
	v_med3_f32 v60, v60, v90, v77
	v_med3_f32 v64, v64, v90, v77
	v_perm_b32 v52, v56, v52, v91
	v_perm_b32 v60, v64, v60, v91
	v_lshl_or_b32 v69, v60, 16, v52
	ds_write_b128 v89, v[66:69] offset:1056
	v_fmamk_f32 v5, v5, 0x44800000, v76
	v_fmamk_f32 v9, v9, 0x44800000, v76
	v_fmamk_f32 v13, v13, 0x44800000, v76
	v_fmamk_f32 v17, v17, 0x44800000, v76
	v_med3_f32 v5, v5, v90, v77
	v_med3_f32 v9, v9, v90, v77
	v_med3_f32 v13, v13, v90, v77
	v_med3_f32 v17, v17, v90, v77
	v_perm_b32 v5, v9, v5, v91
	v_perm_b32 v13, v17, v13, v91
	v_lshl_or_b32 v66, v13, 16, v5
	v_fmamk_f32 v21, v21, 0x44800000, v76
	v_fmamk_f32 v25, v25, 0x44800000, v76
	v_fmamk_f32 v29, v29, 0x44800000, v76
	v_fmamk_f32 v33, v33, 0x44800000, v76
	v_med3_f32 v21, v21, v90, v77
	v_med3_f32 v25, v25, v90, v77
	v_med3_f32 v29, v29, v90, v77
	v_med3_f32 v33, v33, v90, v77
	v_perm_b32 v21, v25, v21, v91
	v_perm_b32 v29, v33, v29, v91
	v_lshl_or_b32 v67, v29, 16, v21
	v_fmamk_f32 v37, v37, 0x44800000, v76
	v_fmamk_f32 v41, v41, 0x44800000, v76
	v_fmamk_f32 v45, v45, 0x44800000, v76
	v_fmamk_f32 v49, v49, 0x44800000, v76
	v_med3_f32 v37, v37, v90, v77
	v_med3_f32 v41, v41, v90, v77
	v_med3_f32 v45, v45, v90, v77
	v_med3_f32 v49, v49, v90, v77
	v_perm_b32 v37, v41, v37, v91
	v_perm_b32 v45, v49, v45, v91
	v_lshl_or_b32 v68, v45, 16, v37
	v_fmamk_f32 v53, v53, 0x44800000, v76
	v_fmamk_f32 v57, v57, 0x44800000, v76
	v_fmamk_f32 v61, v61, 0x44800000, v76
	v_fmamk_f32 v65, v65, 0x44800000, v76
	v_med3_f32 v53, v53, v90, v77
	v_med3_f32 v57, v57, v90, v77
	v_med3_f32 v61, v61, v90, v77
	v_med3_f32 v65, v65, v90, v77
	v_perm_b32 v53, v57, v53, v91
	v_perm_b32 v61, v65, v61, v91
	v_lshl_or_b32 v69, v61, 16, v53
	ds_write_b128 v89, v[66:69] offset:1584
	s_mov_b64 s[28:29], 0

.LBB0_2106:
	s_mov_b32 s69, s25
	s_mov_b32 s19, s80
	s_mov_b32 s68, s83
	s_mov_b32 s11, s23
	s_mov_b32 s18, s24
	s_mov_b32 s10, s22
	s_mov_b64 s[76:77], s[78:79]
	s_mov_b64 s[30:31], -1
	s_mov_b64 s[2:3], 0
	s_cmp_lt_i32 s25, 2
	s_mov_b64 s[28:29], 0
	s_cbranch_scc1 .LBB0_2113
	s_cmp_eq_u32 s69, 2
	s_mov_b64 s[28:29], -1
	s_cbranch_scc0 .LBB0_2109
	s_waitcnt vmcnt(0)
	v_mov_b32_e32 v77, 0x4b400000
	v_mov_b32_e32 v79, 0x4b40007f
	v_mov_b32_e32 v83, 0x4b3fff81
	v_mov_b32_e32 v84, 0xc0c0400
	v_add_u32_e32 v74, v199, v198
	v_fmamk_f32 v2, v2, 0x44800000, v77
	v_fmamk_f32 v6, v6, 0x44800000, v77
	v_fmamk_f32 v10, v10, 0x44800000, v77
	v_fmamk_f32 v14, v14, 0x44800000, v77
	v_med3_f32 v2, v2, v83, v79
	v_med3_f32 v6, v6, v83, v79
	v_med3_f32 v10, v10, v83, v79
	v_med3_f32 v14, v14, v83, v79
	v_perm_b32 v2, v6, v2, v84
	v_perm_b32 v10, v14, v10, v84
	v_lshl_or_b32 v66, v10, 16, v2
	v_fmamk_f32 v18, v18, 0x44800000, v77
	v_fmamk_f32 v22, v22, 0x44800000, v77
	v_fmamk_f32 v26, v26, 0x44800000, v77
	v_fmamk_f32 v30, v30, 0x44800000, v77
	v_med3_f32 v18, v18, v83, v79
	v_med3_f32 v22, v22, v83, v79
	v_med3_f32 v26, v26, v83, v79
	v_med3_f32 v30, v30, v83, v79
	v_perm_b32 v18, v22, v18, v84
	v_perm_b32 v26, v30, v26, v84
	v_lshl_or_b32 v67, v26, 16, v18
	v_fmamk_f32 v34, v34, 0x44800000, v77
	v_fmamk_f32 v38, v38, 0x44800000, v77
	v_fmamk_f32 v42, v42, 0x44800000, v77
	v_fmamk_f32 v46, v46, 0x44800000, v77
	v_med3_f32 v34, v34, v83, v79
	v_med3_f32 v38, v38, v83, v79
	v_med3_f32 v42, v42, v83, v79
	v_med3_f32 v46, v46, v83, v79
	v_perm_b32 v34, v38, v34, v84
	v_perm_b32 v42, v46, v42, v84
	v_lshl_or_b32 v68, v42, 16, v34
	v_fmamk_f32 v50, v50, 0x44800000, v77
	v_fmamk_f32 v54, v54, 0x44800000, v77
	v_fmamk_f32 v58, v58, 0x44800000, v77
	v_fmamk_f32 v62, v62, 0x44800000, v77
	v_med3_f32 v50, v50, v83, v79
	v_med3_f32 v54, v54, v83, v79
	v_med3_f32 v58, v58, v83, v79
	v_med3_f32 v62, v62, v83, v79
	v_perm_b32 v50, v54, v50, v84
	v_perm_b32 v58, v62, v58, v84
	v_lshl_or_b32 v69, v58, 16, v50
	ds_write_b128 v74, v[66:69]
	v_fmamk_f32 v3, v3, 0x44800000, v77
	v_fmamk_f32 v7, v7, 0x44800000, v77
	v_fmamk_f32 v11, v11, 0x44800000, v77
	v_fmamk_f32 v15, v15, 0x44800000, v77
	v_med3_f32 v3, v3, v83, v79
	v_med3_f32 v7, v7, v83, v79
	v_med3_f32 v11, v11, v83, v79
	v_med3_f32 v15, v15, v83, v79
	v_perm_b32 v3, v7, v3, v84
	v_perm_b32 v11, v15, v11, v84
	v_lshl_or_b32 v66, v11, 16, v3
	v_fmamk_f32 v19, v19, 0x44800000, v77
	v_fmamk_f32 v23, v23, 0x44800000, v77
	v_fmamk_f32 v27, v27, 0x44800000, v77
	v_fmamk_f32 v31, v31, 0x44800000, v77
	v_med3_f32 v19, v19, v83, v79
	v_med3_f32 v23, v23, v83, v79
	v_med3_f32 v27, v27, v83, v79
	v_med3_f32 v31, v31, v83, v79
	v_perm_b32 v19, v23, v19, v84
	v_perm_b32 v27, v31, v27, v84
	v_lshl_or_b32 v67, v27, 16, v19
	v_fmamk_f32 v35, v35, 0x44800000, v77
	v_fmamk_f32 v39, v39, 0x44800000, v77
	v_fmamk_f32 v43, v43, 0x44800000, v77
	v_fmamk_f32 v47, v47, 0x44800000, v77
	v_med3_f32 v35, v35, v83, v79
	v_med3_f32 v39, v39, v83, v79
	v_med3_f32 v43, v43, v83, v79
	v_med3_f32 v47, v47, v83, v79
	v_perm_b32 v35, v39, v35, v84
	v_perm_b32 v43, v47, v43, v84
	v_lshl_or_b32 v68, v43, 16, v35
	v_fmamk_f32 v51, v51, 0x44800000, v77
	v_fmamk_f32 v55, v55, 0x44800000, v77
	v_fmamk_f32 v59, v59, 0x44800000, v77
	v_fmamk_f32 v63, v63, 0x44800000, v77
	v_med3_f32 v51, v51, v83, v79
	v_med3_f32 v55, v55, v83, v79
	v_med3_f32 v59, v59, v83, v79
	v_med3_f32 v63, v63, v83, v79
	v_perm_b32 v51, v55, v51, v84
	v_perm_b32 v59, v63, v59, v84
	v_lshl_or_b32 v69, v59, 16, v51
	ds_write_b128 v74, v[66:69] offset:528
	v_fmamk_f32 v4, v4, 0x44800000, v77
	v_fmamk_f32 v8, v8, 0x44800000, v77
	v_fmamk_f32 v12, v12, 0x44800000, v77
	v_fmamk_f32 v16, v16, 0x44800000, v77
	v_med3_f32 v4, v4, v83, v79
	v_med3_f32 v8, v8, v83, v79
	v_med3_f32 v12, v12, v83, v79
	v_med3_f32 v16, v16, v83, v79
	v_perm_b32 v4, v8, v4, v84
	v_perm_b32 v12, v16, v12, v84
	v_lshl_or_b32 v66, v12, 16, v4
	v_fmamk_f32 v20, v20, 0x44800000, v77
	v_fmamk_f32 v24, v24, 0x44800000, v77
	v_fmamk_f32 v28, v28, 0x44800000, v77
	v_fmamk_f32 v32, v32, 0x44800000, v77
	v_med3_f32 v20, v20, v83, v79
	v_med3_f32 v24, v24, v83, v79
	v_med3_f32 v28, v28, v83, v79
	v_med3_f32 v32, v32, v83, v79
	v_perm_b32 v20, v24, v20, v84
	v_perm_b32 v28, v32, v28, v84
	v_lshl_or_b32 v67, v28, 16, v20
	v_fmamk_f32 v36, v36, 0x44800000, v77
	v_fmamk_f32 v40, v40, 0x44800000, v77
	v_fmamk_f32 v44, v44, 0x44800000, v77
	v_fmamk_f32 v48, v48, 0x44800000, v77
	v_med3_f32 v36, v36, v83, v79
	v_med3_f32 v40, v40, v83, v79
	v_med3_f32 v44, v44, v83, v79
	v_med3_f32 v48, v48, v83, v79
	v_perm_b32 v36, v40, v36, v84
	v_perm_b32 v44, v48, v44, v84
	v_lshl_or_b32 v68, v44, 16, v36
	v_fmamk_f32 v52, v52, 0x44800000, v77
	v_fmamk_f32 v56, v56, 0x44800000, v77
	v_fmamk_f32 v60, v60, 0x44800000, v77
	v_fmamk_f32 v64, v64, 0x44800000, v77
	v_med3_f32 v52, v52, v83, v79
	v_med3_f32 v56, v56, v83, v79
	v_med3_f32 v60, v60, v83, v79
	v_med3_f32 v64, v64, v83, v79
	v_perm_b32 v52, v56, v52, v84
	v_perm_b32 v60, v64, v60, v84
	v_lshl_or_b32 v69, v60, 16, v52
	ds_write_b128 v74, v[66:69] offset:1056
	v_fmamk_f32 v5, v5, 0x44800000, v77
	v_fmamk_f32 v9, v9, 0x44800000, v77
	v_fmamk_f32 v13, v13, 0x44800000, v77
	v_fmamk_f32 v17, v17, 0x44800000, v77
	v_med3_f32 v5, v5, v83, v79
	v_med3_f32 v9, v9, v83, v79
	v_med3_f32 v13, v13, v83, v79
	v_med3_f32 v17, v17, v83, v79
	v_perm_b32 v5, v9, v5, v84
	v_perm_b32 v13, v17, v13, v84
	v_lshl_or_b32 v66, v13, 16, v5
	v_fmamk_f32 v21, v21, 0x44800000, v77
	v_fmamk_f32 v25, v25, 0x44800000, v77
	v_fmamk_f32 v29, v29, 0x44800000, v77
	v_fmamk_f32 v33, v33, 0x44800000, v77
	v_med3_f32 v21, v21, v83, v79
	v_med3_f32 v25, v25, v83, v79
	v_med3_f32 v29, v29, v83, v79
	v_med3_f32 v33, v33, v83, v79
	v_perm_b32 v21, v25, v21, v84
	v_perm_b32 v29, v33, v29, v84
	v_lshl_or_b32 v67, v29, 16, v21
	v_fmamk_f32 v37, v37, 0x44800000, v77
	v_fmamk_f32 v41, v41, 0x44800000, v77
	v_fmamk_f32 v45, v45, 0x44800000, v77
	v_fmamk_f32 v49, v49, 0x44800000, v77
	v_med3_f32 v37, v37, v83, v79
	v_med3_f32 v41, v41, v83, v79
	v_med3_f32 v45, v45, v83, v79
	v_med3_f32 v49, v49, v83, v79
	v_perm_b32 v37, v41, v37, v84
	v_perm_b32 v45, v49, v45, v84
	v_lshl_or_b32 v68, v45, 16, v37
	v_fmamk_f32 v53, v53, 0x44800000, v77
	v_fmamk_f32 v57, v57, 0x44800000, v77
	v_fmamk_f32 v61, v61, 0x44800000, v77
	v_fmamk_f32 v65, v65, 0x44800000, v77
	v_med3_f32 v53, v53, v83, v79
	v_med3_f32 v57, v57, v83, v79
	v_med3_f32 v61, v61, v83, v79
	v_med3_f32 v65, v65, v83, v79
	v_perm_b32 v53, v57, v53, v84
	v_perm_b32 v61, v65, v61, v84
	v_lshl_or_b32 v69, v61, 16, v53
	ds_write_b128 v74, v[66:69] offset:1584
	s_mov_b64 s[28:29], 0

.LBB0_2347:
	s_mov_b32 s21, s77
	s_mov_b32 s23, s54
	s_mov_b32 s20, s78
	s_mov_b32 s11, s25
	s_mov_b32 s22, s76
	s_mov_b32 s10, s24
	s_mov_b64 s[26:27], s[52:53]
	s_mov_b64 s[30:31], -1
	s_mov_b64 s[2:3], 0
	s_cmp_lt_i32 s77, 2
	s_mov_b64 s[28:29], 0
	s_cbranch_scc1 .LBB0_2354
	s_cmp_eq_u32 s21, 2
	s_mov_b64 s[28:29], -1
	s_cbranch_scc0 .LBB0_2350
	s_waitcnt vmcnt(0)
	v_mov_b32_e32 v73, 0x4b400000
	v_mov_b32_e32 v74, 0x4b40007f
	v_mov_b32_e32 v75, 0x4b3fff81
	v_mov_b32_e32 v76, 0xc0c0400
	v_add_u32_e32 v70, v199, v198
	v_fmamk_f32 v2, v2, 0x44800000, v73
	v_fmamk_f32 v6, v6, 0x44800000, v73
	v_fmamk_f32 v10, v10, 0x44800000, v73
	v_fmamk_f32 v14, v14, 0x44800000, v73
	v_med3_f32 v2, v2, v75, v74
	v_med3_f32 v6, v6, v75, v74
	v_med3_f32 v10, v10, v75, v74
	v_med3_f32 v14, v14, v75, v74
	v_perm_b32 v2, v6, v2, v76
	v_perm_b32 v10, v14, v10, v76
	v_lshl_or_b32 v66, v10, 16, v2
	v_fmamk_f32 v18, v18, 0x44800000, v73
	v_fmamk_f32 v22, v22, 0x44800000, v73
	v_fmamk_f32 v26, v26, 0x44800000, v73
	v_fmamk_f32 v30, v30, 0x44800000, v73
	v_med3_f32 v18, v18, v75, v74
	v_med3_f32 v22, v22, v75, v74
	v_med3_f32 v26, v26, v75, v74
	v_med3_f32 v30, v30, v75, v74
	v_perm_b32 v18, v22, v18, v76
	v_perm_b32 v26, v30, v26, v76
	v_lshl_or_b32 v67, v26, 16, v18
	v_fmamk_f32 v34, v34, 0x44800000, v73
	v_fmamk_f32 v38, v38, 0x44800000, v73
	v_fmamk_f32 v42, v42, 0x44800000, v73
	v_fmamk_f32 v46, v46, 0x44800000, v73
	v_med3_f32 v34, v34, v75, v74
	v_med3_f32 v38, v38, v75, v74
	v_med3_f32 v42, v42, v75, v74
	v_med3_f32 v46, v46, v75, v74
	v_perm_b32 v34, v38, v34, v76
	v_perm_b32 v42, v46, v42, v76
	v_lshl_or_b32 v68, v42, 16, v34
	v_fmamk_f32 v50, v50, 0x44800000, v73
	v_fmamk_f32 v54, v54, 0x44800000, v73
	v_fmamk_f32 v58, v58, 0x44800000, v73
	v_fmamk_f32 v62, v62, 0x44800000, v73
	v_med3_f32 v50, v50, v75, v74
	v_med3_f32 v54, v54, v75, v74
	v_med3_f32 v58, v58, v75, v74
	v_med3_f32 v62, v62, v75, v74
	v_perm_b32 v50, v54, v50, v76
	v_perm_b32 v58, v62, v58, v76
	v_lshl_or_b32 v69, v58, 16, v50
	ds_write_b128 v70, v[66:69]
	v_fmamk_f32 v3, v3, 0x44800000, v73
	v_fmamk_f32 v7, v7, 0x44800000, v73
	v_fmamk_f32 v11, v11, 0x44800000, v73
	v_fmamk_f32 v15, v15, 0x44800000, v73
	v_med3_f32 v3, v3, v75, v74
	v_med3_f32 v7, v7, v75, v74
	v_med3_f32 v11, v11, v75, v74
	v_med3_f32 v15, v15, v75, v74
	v_perm_b32 v3, v7, v3, v76
	v_perm_b32 v11, v15, v11, v76
	v_lshl_or_b32 v66, v11, 16, v3
	v_fmamk_f32 v19, v19, 0x44800000, v73
	v_fmamk_f32 v23, v23, 0x44800000, v73
	v_fmamk_f32 v27, v27, 0x44800000, v73
	v_fmamk_f32 v31, v31, 0x44800000, v73
	v_med3_f32 v19, v19, v75, v74
	v_med3_f32 v23, v23, v75, v74
	v_med3_f32 v27, v27, v75, v74
	v_med3_f32 v31, v31, v75, v74
	v_perm_b32 v19, v23, v19, v76
	v_perm_b32 v27, v31, v27, v76
	v_lshl_or_b32 v67, v27, 16, v19
	v_fmamk_f32 v35, v35, 0x44800000, v73
	v_fmamk_f32 v39, v39, 0x44800000, v73
	v_fmamk_f32 v43, v43, 0x44800000, v73
	v_fmamk_f32 v47, v47, 0x44800000, v73
	v_med3_f32 v35, v35, v75, v74
	v_med3_f32 v39, v39, v75, v74
	v_med3_f32 v43, v43, v75, v74
	v_med3_f32 v47, v47, v75, v74
	v_perm_b32 v35, v39, v35, v76
	v_perm_b32 v43, v47, v43, v76
	v_lshl_or_b32 v68, v43, 16, v35
	v_fmamk_f32 v51, v51, 0x44800000, v73
	v_fmamk_f32 v55, v55, 0x44800000, v73
	v_fmamk_f32 v59, v59, 0x44800000, v73
	v_fmamk_f32 v63, v63, 0x44800000, v73
	v_med3_f32 v51, v51, v75, v74
	v_med3_f32 v55, v55, v75, v74
	v_med3_f32 v59, v59, v75, v74
	v_med3_f32 v63, v63, v75, v74
	v_perm_b32 v51, v55, v51, v76
	v_perm_b32 v59, v63, v59, v76
	v_lshl_or_b32 v69, v59, 16, v51
	ds_write_b128 v70, v[66:69] offset:528
	v_fmamk_f32 v4, v4, 0x44800000, v73
	v_fmamk_f32 v8, v8, 0x44800000, v73
	v_fmamk_f32 v12, v12, 0x44800000, v73
	v_fmamk_f32 v16, v16, 0x44800000, v73
	v_med3_f32 v4, v4, v75, v74
	v_med3_f32 v8, v8, v75, v74
	v_med3_f32 v12, v12, v75, v74
	v_med3_f32 v16, v16, v75, v74
	v_perm_b32 v4, v8, v4, v76
	v_perm_b32 v12, v16, v12, v76
	v_lshl_or_b32 v66, v12, 16, v4
	v_fmamk_f32 v20, v20, 0x44800000, v73
	v_fmamk_f32 v24, v24, 0x44800000, v73
	v_fmamk_f32 v28, v28, 0x44800000, v73
	v_fmamk_f32 v32, v32, 0x44800000, v73
	v_med3_f32 v20, v20, v75, v74
	v_med3_f32 v24, v24, v75, v74
	v_med3_f32 v28, v28, v75, v74
	v_med3_f32 v32, v32, v75, v74
	v_perm_b32 v20, v24, v20, v76
	v_perm_b32 v28, v32, v28, v76
	v_lshl_or_b32 v67, v28, 16, v20
	v_fmamk_f32 v36, v36, 0x44800000, v73
	v_fmamk_f32 v40, v40, 0x44800000, v73
	v_fmamk_f32 v44, v44, 0x44800000, v73
	v_fmamk_f32 v48, v48, 0x44800000, v73
	v_med3_f32 v36, v36, v75, v74
	v_med3_f32 v40, v40, v75, v74
	v_med3_f32 v44, v44, v75, v74
	v_med3_f32 v48, v48, v75, v74
	v_perm_b32 v36, v40, v36, v76
	v_perm_b32 v44, v48, v44, v76
	v_lshl_or_b32 v68, v44, 16, v36
	v_fmamk_f32 v52, v52, 0x44800000, v73
	v_fmamk_f32 v56, v56, 0x44800000, v73
	v_fmamk_f32 v60, v60, 0x44800000, v73
	v_fmamk_f32 v64, v64, 0x44800000, v73
	v_med3_f32 v52, v52, v75, v74
	v_med3_f32 v56, v56, v75, v74
	v_med3_f32 v60, v60, v75, v74
	v_med3_f32 v64, v64, v75, v74
	v_perm_b32 v52, v56, v52, v76
	v_perm_b32 v60, v64, v60, v76
	v_lshl_or_b32 v69, v60, 16, v52
	ds_write_b128 v70, v[66:69] offset:1056
	v_fmamk_f32 v5, v5, 0x44800000, v73
	v_fmamk_f32 v9, v9, 0x44800000, v73
	v_fmamk_f32 v13, v13, 0x44800000, v73
	v_fmamk_f32 v17, v17, 0x44800000, v73
	v_med3_f32 v5, v5, v75, v74
	v_med3_f32 v9, v9, v75, v74
	v_med3_f32 v13, v13, v75, v74
	v_med3_f32 v17, v17, v75, v74
	v_perm_b32 v5, v9, v5, v76
	v_perm_b32 v13, v17, v13, v76
	v_lshl_or_b32 v66, v13, 16, v5
	v_fmamk_f32 v21, v21, 0x44800000, v73
	v_fmamk_f32 v25, v25, 0x44800000, v73
	v_fmamk_f32 v29, v29, 0x44800000, v73
	v_fmamk_f32 v33, v33, 0x44800000, v73
	v_med3_f32 v21, v21, v75, v74
	v_med3_f32 v25, v25, v75, v74
	v_med3_f32 v29, v29, v75, v74
	v_med3_f32 v33, v33, v75, v74
	v_perm_b32 v21, v25, v21, v76
	v_perm_b32 v29, v33, v29, v76
	v_lshl_or_b32 v67, v29, 16, v21
	v_fmamk_f32 v37, v37, 0x44800000, v73
	v_fmamk_f32 v41, v41, 0x44800000, v73
	v_fmamk_f32 v45, v45, 0x44800000, v73
	v_fmamk_f32 v49, v49, 0x44800000, v73
	v_med3_f32 v37, v37, v75, v74
	v_med3_f32 v41, v41, v75, v74
	v_med3_f32 v45, v45, v75, v74
	v_med3_f32 v49, v49, v75, v74
	v_perm_b32 v37, v41, v37, v76
	v_perm_b32 v45, v49, v45, v76
	v_lshl_or_b32 v68, v45, 16, v37
	v_fmamk_f32 v53, v53, 0x44800000, v73
	v_fmamk_f32 v57, v57, 0x44800000, v73
	v_fmamk_f32 v61, v61, 0x44800000, v73
	v_fmamk_f32 v65, v65, 0x44800000, v73
	v_med3_f32 v53, v53, v75, v74
	v_med3_f32 v57, v57, v75, v74
	v_med3_f32 v61, v61, v75, v74
	v_med3_f32 v65, v65, v75, v74
	v_perm_b32 v53, v57, v53, v76
	v_perm_b32 v61, v65, v61, v76
	v_lshl_or_b32 v69, v61, 16, v53
	ds_write_b128 v70, v[66:69] offset:1584
	s_mov_b64 s[28:29], 0

.LBB0_2641:
	s_mov_b32 s21, s76
	s_mov_b32 s23, s54
	s_mov_b32 s20, s77
	s_mov_b32 s11, s25
	s_mov_b32 s22, s71
	s_mov_b32 s10, s24
	s_mov_b64 s[26:27], s[52:53]
	s_mov_b64 s[30:31], -1
	s_mov_b64 s[2:3], 0
	s_cmp_lt_i32 s76, 2
	s_mov_b64 s[28:29], 0
	s_cbranch_scc1 .LBB0_2648
	s_cmp_eq_u32 s21, 2
	s_mov_b64 s[28:29], -1
	s_cbranch_scc0 .LBB0_2644
	s_waitcnt vmcnt(0)
	v_mov_b32_e32 v73, 0x4b400000
	v_mov_b32_e32 v74, 0x4b40007f
	v_mov_b32_e32 v75, 0x4b3fff81
	v_mov_b32_e32 v76, 0xc0c0400
	v_add_u32_e32 v70, v199, v198
	v_fmamk_f32 v2, v2, 0x44800000, v73
	v_fmamk_f32 v6, v6, 0x44800000, v73
	v_fmamk_f32 v10, v10, 0x44800000, v73
	v_fmamk_f32 v14, v14, 0x44800000, v73
	v_med3_f32 v2, v2, v75, v74
	v_med3_f32 v6, v6, v75, v74
	v_med3_f32 v10, v10, v75, v74
	v_med3_f32 v14, v14, v75, v74
	v_perm_b32 v2, v6, v2, v76
	v_perm_b32 v10, v14, v10, v76
	v_lshl_or_b32 v66, v10, 16, v2
	v_fmamk_f32 v18, v18, 0x44800000, v73
	v_fmamk_f32 v22, v22, 0x44800000, v73
	v_fmamk_f32 v26, v26, 0x44800000, v73
	v_fmamk_f32 v30, v30, 0x44800000, v73
	v_med3_f32 v18, v18, v75, v74
	v_med3_f32 v22, v22, v75, v74
	v_med3_f32 v26, v26, v75, v74
	v_med3_f32 v30, v30, v75, v74
	v_perm_b32 v18, v22, v18, v76
	v_perm_b32 v26, v30, v26, v76
	v_lshl_or_b32 v67, v26, 16, v18
	v_fmamk_f32 v34, v34, 0x44800000, v73
	v_fmamk_f32 v38, v38, 0x44800000, v73
	v_fmamk_f32 v42, v42, 0x44800000, v73
	v_fmamk_f32 v46, v46, 0x44800000, v73
	v_med3_f32 v34, v34, v75, v74
	v_med3_f32 v38, v38, v75, v74
	v_med3_f32 v42, v42, v75, v74
	v_med3_f32 v46, v46, v75, v74
	v_perm_b32 v34, v38, v34, v76
	v_perm_b32 v42, v46, v42, v76
	v_lshl_or_b32 v68, v42, 16, v34
	v_fmamk_f32 v50, v50, 0x44800000, v73
	v_fmamk_f32 v54, v54, 0x44800000, v73
	v_fmamk_f32 v58, v58, 0x44800000, v73
	v_fmamk_f32 v62, v62, 0x44800000, v73
	v_med3_f32 v50, v50, v75, v74
	v_med3_f32 v54, v54, v75, v74
	v_med3_f32 v58, v58, v75, v74
	v_med3_f32 v62, v62, v75, v74
	v_perm_b32 v50, v54, v50, v76
	v_perm_b32 v58, v62, v58, v76
	v_lshl_or_b32 v69, v58, 16, v50
	ds_write_b128 v70, v[66:69]
	v_fmamk_f32 v3, v3, 0x44800000, v73
	v_fmamk_f32 v7, v7, 0x44800000, v73
	v_fmamk_f32 v11, v11, 0x44800000, v73
	v_fmamk_f32 v15, v15, 0x44800000, v73
	v_med3_f32 v3, v3, v75, v74
	v_med3_f32 v7, v7, v75, v74
	v_med3_f32 v11, v11, v75, v74
	v_med3_f32 v15, v15, v75, v74
	v_perm_b32 v3, v7, v3, v76
	v_perm_b32 v11, v15, v11, v76
	v_lshl_or_b32 v66, v11, 16, v3
	v_fmamk_f32 v19, v19, 0x44800000, v73
	v_fmamk_f32 v23, v23, 0x44800000, v73
	v_fmamk_f32 v27, v27, 0x44800000, v73
	v_fmamk_f32 v31, v31, 0x44800000, v73
	v_med3_f32 v19, v19, v75, v74
	v_med3_f32 v23, v23, v75, v74
	v_med3_f32 v27, v27, v75, v74
	v_med3_f32 v31, v31, v75, v74
	v_perm_b32 v19, v23, v19, v76
	v_perm_b32 v27, v31, v27, v76
	v_lshl_or_b32 v67, v27, 16, v19
	v_fmamk_f32 v35, v35, 0x44800000, v73
	v_fmamk_f32 v39, v39, 0x44800000, v73
	v_fmamk_f32 v43, v43, 0x44800000, v73
	v_fmamk_f32 v47, v47, 0x44800000, v73
	v_med3_f32 v35, v35, v75, v74
	v_med3_f32 v39, v39, v75, v74
	v_med3_f32 v43, v43, v75, v74
	v_med3_f32 v47, v47, v75, v74
	v_perm_b32 v35, v39, v35, v76
	v_perm_b32 v43, v47, v43, v76
	v_lshl_or_b32 v68, v43, 16, v35
	v_fmamk_f32 v51, v51, 0x44800000, v73
	v_fmamk_f32 v55, v55, 0x44800000, v73
	v_fmamk_f32 v59, v59, 0x44800000, v73
	v_fmamk_f32 v63, v63, 0x44800000, v73
	v_med3_f32 v51, v51, v75, v74
	v_med3_f32 v55, v55, v75, v74
	v_med3_f32 v59, v59, v75, v74
	v_med3_f32 v63, v63, v75, v74
	v_perm_b32 v51, v55, v51, v76
	v_perm_b32 v59, v63, v59, v76
	v_lshl_or_b32 v69, v59, 16, v51
	ds_write_b128 v70, v[66:69] offset:528
	v_fmamk_f32 v4, v4, 0x44800000, v73
	v_fmamk_f32 v8, v8, 0x44800000, v73
	v_fmamk_f32 v12, v12, 0x44800000, v73
	v_fmamk_f32 v16, v16, 0x44800000, v73
	v_med3_f32 v4, v4, v75, v74
	v_med3_f32 v8, v8, v75, v74
	v_med3_f32 v12, v12, v75, v74
	v_med3_f32 v16, v16, v75, v74
	v_perm_b32 v4, v8, v4, v76
	v_perm_b32 v12, v16, v12, v76
	v_lshl_or_b32 v66, v12, 16, v4
	v_fmamk_f32 v20, v20, 0x44800000, v73
	v_fmamk_f32 v24, v24, 0x44800000, v73
	v_fmamk_f32 v28, v28, 0x44800000, v73
	v_fmamk_f32 v32, v32, 0x44800000, v73
	v_med3_f32 v20, v20, v75, v74
	v_med3_f32 v24, v24, v75, v74
	v_med3_f32 v28, v28, v75, v74
	v_med3_f32 v32, v32, v75, v74
	v_perm_b32 v20, v24, v20, v76
	v_perm_b32 v28, v32, v28, v76
	v_lshl_or_b32 v67, v28, 16, v20
	v_fmamk_f32 v36, v36, 0x44800000, v73
	v_fmamk_f32 v40, v40, 0x44800000, v73
	v_fmamk_f32 v44, v44, 0x44800000, v73
	v_fmamk_f32 v48, v48, 0x44800000, v73
	v_med3_f32 v36, v36, v75, v74
	v_med3_f32 v40, v40, v75, v74
	v_med3_f32 v44, v44, v75, v74
	v_med3_f32 v48, v48, v75, v74
	v_perm_b32 v36, v40, v36, v76
	v_perm_b32 v44, v48, v44, v76
	v_lshl_or_b32 v68, v44, 16, v36
	v_fmamk_f32 v52, v52, 0x44800000, v73
	v_fmamk_f32 v56, v56, 0x44800000, v73
	v_fmamk_f32 v60, v60, 0x44800000, v73
	v_fmamk_f32 v64, v64, 0x44800000, v73
	v_med3_f32 v52, v52, v75, v74
	v_med3_f32 v56, v56, v75, v74
	v_med3_f32 v60, v60, v75, v74
	v_med3_f32 v64, v64, v75, v74
	v_perm_b32 v52, v56, v52, v76
	v_perm_b32 v60, v64, v60, v76
	v_lshl_or_b32 v69, v60, 16, v52
	ds_write_b128 v70, v[66:69] offset:1056
	v_fmamk_f32 v5, v5, 0x44800000, v73
	v_fmamk_f32 v9, v9, 0x44800000, v73
	v_fmamk_f32 v13, v13, 0x44800000, v73
	v_fmamk_f32 v17, v17, 0x44800000, v73
	v_med3_f32 v5, v5, v75, v74
	v_med3_f32 v9, v9, v75, v74
	v_med3_f32 v13, v13, v75, v74
	v_med3_f32 v17, v17, v75, v74
	v_perm_b32 v5, v9, v5, v76
	v_perm_b32 v13, v17, v13, v76
	v_lshl_or_b32 v66, v13, 16, v5
	v_fmamk_f32 v21, v21, 0x44800000, v73
	v_fmamk_f32 v25, v25, 0x44800000, v73
	v_fmamk_f32 v29, v29, 0x44800000, v73
	v_fmamk_f32 v33, v33, 0x44800000, v73
	v_med3_f32 v21, v21, v75, v74
	v_med3_f32 v25, v25, v75, v74
	v_med3_f32 v29, v29, v75, v74
	v_med3_f32 v33, v33, v75, v74
	v_perm_b32 v21, v25, v21, v76
	v_perm_b32 v29, v33, v29, v76
	v_lshl_or_b32 v67, v29, 16, v21
	v_fmamk_f32 v37, v37, 0x44800000, v73
	v_fmamk_f32 v41, v41, 0x44800000, v73
	v_fmamk_f32 v45, v45, 0x44800000, v73
	v_fmamk_f32 v49, v49, 0x44800000, v73
	v_med3_f32 v37, v37, v75, v74
	v_med3_f32 v41, v41, v75, v74
	v_med3_f32 v45, v45, v75, v74
	v_med3_f32 v49, v49, v75, v74
	v_perm_b32 v37, v41, v37, v76
	v_perm_b32 v45, v49, v45, v76
	v_lshl_or_b32 v68, v45, 16, v37
	v_fmamk_f32 v53, v53, 0x44800000, v73
	v_fmamk_f32 v57, v57, 0x44800000, v73
	v_fmamk_f32 v61, v61, 0x44800000, v73
	v_fmamk_f32 v65, v65, 0x44800000, v73
	v_med3_f32 v53, v53, v75, v74
	v_med3_f32 v57, v57, v75, v74
	v_med3_f32 v61, v61, v75, v74
	v_med3_f32 v65, v65, v75, v74
	v_perm_b32 v53, v57, v53, v76
	v_perm_b32 v61, v65, v61, v76
	v_lshl_or_b32 v69, v61, 16, v53
	ds_write_b128 v70, v[66:69] offset:1584
	s_mov_b64 s[28:29], 0

.LBB0_3185:
	s_mov_b32 s17, s68
	s_mov_b32 s64, s22
	s_mov_b32 s16, s69
	s_mov_b32 s25, s66
	s_mov_b32 s63, s67
	s_mov_b32 s24, s65
	s_mov_b64 s[18:19], s[20:21]
	s_mov_b64 s[22:23], -1
	s_mov_b64 s[2:3], 0
	s_cmp_lt_i32 s68, 2
	s_mov_b64 s[20:21], 0
	s_cbranch_scc1 .LBB0_3192
	s_cmp_eq_u32 s17, 2
	s_mov_b64 s[20:21], -1
	s_cbranch_scc0 .LBB0_3188
	s_waitcnt vmcnt(0)
	v_mov_b32_e32 v76, 0x4b400000
	v_mov_b32_e32 v77, 0x4b40007f
	v_mov_b32_e32 v90, 0x4b3fff81
	v_mov_b32_e32 v91, 0xc0c0400
	v_add_u32_e32 v89, v78, v75
	v_fmamk_f32 v2, v2, 0x44800000, v76
	v_fmamk_f32 v6, v6, 0x44800000, v76
	v_fmamk_f32 v10, v10, 0x44800000, v76
	v_fmamk_f32 v14, v14, 0x44800000, v76
	v_med3_f32 v2, v2, v90, v77
	v_med3_f32 v6, v6, v90, v77
	v_med3_f32 v10, v10, v90, v77
	v_med3_f32 v14, v14, v90, v77
	v_perm_b32 v2, v6, v2, v91
	v_perm_b32 v10, v14, v10, v91
	v_lshl_or_b32 v66, v10, 16, v2
	v_fmamk_f32 v18, v18, 0x44800000, v76
	v_fmamk_f32 v22, v22, 0x44800000, v76
	v_fmamk_f32 v26, v26, 0x44800000, v76
	v_fmamk_f32 v30, v30, 0x44800000, v76
	v_med3_f32 v18, v18, v90, v77
	v_med3_f32 v22, v22, v90, v77
	v_med3_f32 v26, v26, v90, v77
	v_med3_f32 v30, v30, v90, v77
	v_perm_b32 v18, v22, v18, v91
	v_perm_b32 v26, v30, v26, v91
	v_lshl_or_b32 v67, v26, 16, v18
	v_fmamk_f32 v34, v34, 0x44800000, v76
	v_fmamk_f32 v38, v38, 0x44800000, v76
	v_fmamk_f32 v42, v42, 0x44800000, v76
	v_fmamk_f32 v46, v46, 0x44800000, v76
	v_med3_f32 v34, v34, v90, v77
	v_med3_f32 v38, v38, v90, v77
	v_med3_f32 v42, v42, v90, v77
	v_med3_f32 v46, v46, v90, v77
	v_perm_b32 v34, v38, v34, v91
	v_perm_b32 v42, v46, v42, v91
	v_lshl_or_b32 v68, v42, 16, v34
	v_fmamk_f32 v50, v50, 0x44800000, v76
	v_fmamk_f32 v54, v54, 0x44800000, v76
	v_fmamk_f32 v58, v58, 0x44800000, v76
	v_fmamk_f32 v62, v62, 0x44800000, v76
	v_med3_f32 v50, v50, v90, v77
	v_med3_f32 v54, v54, v90, v77
	v_med3_f32 v58, v58, v90, v77
	v_med3_f32 v62, v62, v90, v77
	v_perm_b32 v50, v54, v50, v91
	v_perm_b32 v58, v62, v58, v91
	v_lshl_or_b32 v69, v58, 16, v50
	ds_write_b128 v89, v[66:69]
	v_fmamk_f32 v3, v3, 0x44800000, v76
	v_fmamk_f32 v7, v7, 0x44800000, v76
	v_fmamk_f32 v11, v11, 0x44800000, v76
	v_fmamk_f32 v15, v15, 0x44800000, v76
	v_med3_f32 v3, v3, v90, v77
	v_med3_f32 v7, v7, v90, v77
	v_med3_f32 v11, v11, v90, v77
	v_med3_f32 v15, v15, v90, v77
	v_perm_b32 v3, v7, v3, v91
	v_perm_b32 v11, v15, v11, v91
	v_lshl_or_b32 v66, v11, 16, v3
	v_fmamk_f32 v19, v19, 0x44800000, v76
	v_fmamk_f32 v23, v23, 0x44800000, v76
	v_fmamk_f32 v27, v27, 0x44800000, v76
	v_fmamk_f32 v31, v31, 0x44800000, v76
	v_med3_f32 v19, v19, v90, v77
	v_med3_f32 v23, v23, v90, v77
	v_med3_f32 v27, v27, v90, v77
	v_med3_f32 v31, v31, v90, v77
	v_perm_b32 v19, v23, v19, v91
	v_perm_b32 v27, v31, v27, v91
	v_lshl_or_b32 v67, v27, 16, v19
	v_fmamk_f32 v35, v35, 0x44800000, v76
	v_fmamk_f32 v39, v39, 0x44800000, v76
	v_fmamk_f32 v43, v43, 0x44800000, v76
	v_fmamk_f32 v47, v47, 0x44800000, v76
	v_med3_f32 v35, v35, v90, v77
	v_med3_f32 v39, v39, v90, v77
	v_med3_f32 v43, v43, v90, v77
	v_med3_f32 v47, v47, v90, v77
	v_perm_b32 v35, v39, v35, v91
	v_perm_b32 v43, v47, v43, v91
	v_lshl_or_b32 v68, v43, 16, v35
	v_fmamk_f32 v51, v51, 0x44800000, v76
	v_fmamk_f32 v55, v55, 0x44800000, v76
	v_fmamk_f32 v59, v59, 0x44800000, v76
	v_fmamk_f32 v63, v63, 0x44800000, v76
	v_med3_f32 v51, v51, v90, v77
	v_med3_f32 v55, v55, v90, v77
	v_med3_f32 v59, v59, v90, v77
	v_med3_f32 v63, v63, v90, v77
	v_perm_b32 v51, v55, v51, v91
	v_perm_b32 v59, v63, v59, v91
	v_lshl_or_b32 v69, v59, 16, v51
	ds_write_b128 v89, v[66:69] offset:528
	v_fmamk_f32 v4, v4, 0x44800000, v76
	v_fmamk_f32 v8, v8, 0x44800000, v76
	v_fmamk_f32 v12, v12, 0x44800000, v76
	v_fmamk_f32 v16, v16, 0x44800000, v76
	v_med3_f32 v4, v4, v90, v77
	v_med3_f32 v8, v8, v90, v77
	v_med3_f32 v12, v12, v90, v77
	v_med3_f32 v16, v16, v90, v77
	v_perm_b32 v4, v8, v4, v91
	v_perm_b32 v12, v16, v12, v91
	v_lshl_or_b32 v66, v12, 16, v4
	v_fmamk_f32 v20, v20, 0x44800000, v76
	v_fmamk_f32 v24, v24, 0x44800000, v76
	v_fmamk_f32 v28, v28, 0x44800000, v76
	v_fmamk_f32 v32, v32, 0x44800000, v76
	v_med3_f32 v20, v20, v90, v77
	v_med3_f32 v24, v24, v90, v77
	v_med3_f32 v28, v28, v90, v77
	v_med3_f32 v32, v32, v90, v77
	v_perm_b32 v20, v24, v20, v91
	v_perm_b32 v28, v32, v28, v91
	v_lshl_or_b32 v67, v28, 16, v20
	v_fmamk_f32 v36, v36, 0x44800000, v76
	v_fmamk_f32 v40, v40, 0x44800000, v76
	v_fmamk_f32 v44, v44, 0x44800000, v76
	v_fmamk_f32 v48, v48, 0x44800000, v76
	v_med3_f32 v36, v36, v90, v77
	v_med3_f32 v40, v40, v90, v77
	v_med3_f32 v44, v44, v90, v77
	v_med3_f32 v48, v48, v90, v77
	v_perm_b32 v36, v40, v36, v91
	v_perm_b32 v44, v48, v44, v91
	v_lshl_or_b32 v68, v44, 16, v36
	v_fmamk_f32 v52, v52, 0x44800000, v76
	v_fmamk_f32 v56, v56, 0x44800000, v76
	v_fmamk_f32 v60, v60, 0x44800000, v76
	v_fmamk_f32 v64, v64, 0x44800000, v76
	v_med3_f32 v52, v52, v90, v77
	v_med3_f32 v56, v56, v90, v77
	v_med3_f32 v60, v60, v90, v77
	v_med3_f32 v64, v64, v90, v77
	v_perm_b32 v52, v56, v52, v91
	v_perm_b32 v60, v64, v60, v91
	v_lshl_or_b32 v69, v60, 16, v52
	ds_write_b128 v89, v[66:69] offset:1056
	v_fmamk_f32 v5, v5, 0x44800000, v76
	v_fmamk_f32 v9, v9, 0x44800000, v76
	v_fmamk_f32 v13, v13, 0x44800000, v76
	v_fmamk_f32 v17, v17, 0x44800000, v76
	v_med3_f32 v5, v5, v90, v77
	v_med3_f32 v9, v9, v90, v77
	v_med3_f32 v13, v13, v90, v77
	v_med3_f32 v17, v17, v90, v77
	v_perm_b32 v5, v9, v5, v91
	v_perm_b32 v13, v17, v13, v91
	v_lshl_or_b32 v66, v13, 16, v5
	v_fmamk_f32 v21, v21, 0x44800000, v76
	v_fmamk_f32 v25, v25, 0x44800000, v76
	v_fmamk_f32 v29, v29, 0x44800000, v76
	v_fmamk_f32 v33, v33, 0x44800000, v76
	v_med3_f32 v21, v21, v90, v77
	v_med3_f32 v25, v25, v90, v77
	v_med3_f32 v29, v29, v90, v77
	v_med3_f32 v33, v33, v90, v77
	v_perm_b32 v21, v25, v21, v91
	v_perm_b32 v29, v33, v29, v91
	v_lshl_or_b32 v67, v29, 16, v21
	v_fmamk_f32 v37, v37, 0x44800000, v76
	v_fmamk_f32 v41, v41, 0x44800000, v76
	v_fmamk_f32 v45, v45, 0x44800000, v76
	v_fmamk_f32 v49, v49, 0x44800000, v76
	v_med3_f32 v37, v37, v90, v77
	v_med3_f32 v41, v41, v90, v77
	v_med3_f32 v45, v45, v90, v77
	v_med3_f32 v49, v49, v90, v77
	v_perm_b32 v37, v41, v37, v91
	v_perm_b32 v45, v49, v45, v91
	v_lshl_or_b32 v68, v45, 16, v37
	v_fmamk_f32 v53, v53, 0x44800000, v76
	v_fmamk_f32 v57, v57, 0x44800000, v76
	v_fmamk_f32 v61, v61, 0x44800000, v76
	v_fmamk_f32 v65, v65, 0x44800000, v76
	v_med3_f32 v53, v53, v90, v77
	v_med3_f32 v57, v57, v90, v77
	v_med3_f32 v61, v61, v90, v77
	v_med3_f32 v65, v65, v90, v77
	v_perm_b32 v53, v57, v53, v91
	v_perm_b32 v61, v65, v61, v91
	v_lshl_or_b32 v69, v61, 16, v53
	ds_write_b128 v89, v[66:69] offset:1584
	s_mov_b64 s[20:21], 0

.LBB0_3427:
	s_mov_b32 s15, s65
	s_mov_b32 s61, s20
	s_mov_b32 s14, s66
	s_mov_b32 s25, s63
	s_mov_b32 s60, s64
	s_mov_b32 s24, s62
	s_mov_b64 s[16:17], s[18:19]
	s_mov_b64 s[20:21], -1
	s_mov_b64 s[2:3], 0
	s_cmp_lt_i32 s65, 2
	s_mov_b64 s[18:19], 0
	s_cbranch_scc1 .LBB0_3434
	s_cmp_eq_u32 s15, 2
	s_mov_b64 s[18:19], -1
	s_cbranch_scc0 .LBB0_3430
	s_waitcnt vmcnt(0)
	v_mov_b32_e32 v76, 0x4b400000
	v_mov_b32_e32 v77, 0x4b40007f
	v_mov_b32_e32 v90, 0x4b3fff81
	v_mov_b32_e32 v91, 0xc0c0400
	v_add_u32_e32 v89, v78, v75
	v_fmamk_f32 v2, v2, 0x44800000, v76
	v_fmamk_f32 v6, v6, 0x44800000, v76
	v_fmamk_f32 v10, v10, 0x44800000, v76
	v_fmamk_f32 v14, v14, 0x44800000, v76
	v_med3_f32 v2, v2, v90, v77
	v_med3_f32 v6, v6, v90, v77
	v_med3_f32 v10, v10, v90, v77
	v_med3_f32 v14, v14, v90, v77
	v_perm_b32 v2, v6, v2, v91
	v_perm_b32 v10, v14, v10, v91
	v_lshl_or_b32 v66, v10, 16, v2
	v_fmamk_f32 v18, v18, 0x44800000, v76
	v_fmamk_f32 v22, v22, 0x44800000, v76
	v_fmamk_f32 v26, v26, 0x44800000, v76
	v_fmamk_f32 v30, v30, 0x44800000, v76
	v_med3_f32 v18, v18, v90, v77
	v_med3_f32 v22, v22, v90, v77
	v_med3_f32 v26, v26, v90, v77
	v_med3_f32 v30, v30, v90, v77
	v_perm_b32 v18, v22, v18, v91
	v_perm_b32 v26, v30, v26, v91
	v_lshl_or_b32 v67, v26, 16, v18
	v_fmamk_f32 v34, v34, 0x44800000, v76
	v_fmamk_f32 v38, v38, 0x44800000, v76
	v_fmamk_f32 v42, v42, 0x44800000, v76
	v_fmamk_f32 v46, v46, 0x44800000, v76
	v_med3_f32 v34, v34, v90, v77
	v_med3_f32 v38, v38, v90, v77
	v_med3_f32 v42, v42, v90, v77
	v_med3_f32 v46, v46, v90, v77
	v_perm_b32 v34, v38, v34, v91
	v_perm_b32 v42, v46, v42, v91
	v_lshl_or_b32 v68, v42, 16, v34
	v_fmamk_f32 v50, v50, 0x44800000, v76
	v_fmamk_f32 v54, v54, 0x44800000, v76
	v_fmamk_f32 v58, v58, 0x44800000, v76
	v_fmamk_f32 v62, v62, 0x44800000, v76
	v_med3_f32 v50, v50, v90, v77
	v_med3_f32 v54, v54, v90, v77
	v_med3_f32 v58, v58, v90, v77
	v_med3_f32 v62, v62, v90, v77
	v_perm_b32 v50, v54, v50, v91
	v_perm_b32 v58, v62, v58, v91
	v_lshl_or_b32 v69, v58, 16, v50
	ds_write_b128 v89, v[66:69]
	v_fmamk_f32 v3, v3, 0x44800000, v76
	v_fmamk_f32 v7, v7, 0x44800000, v76
	v_fmamk_f32 v11, v11, 0x44800000, v76
	v_fmamk_f32 v15, v15, 0x44800000, v76
	v_med3_f32 v3, v3, v90, v77
	v_med3_f32 v7, v7, v90, v77
	v_med3_f32 v11, v11, v90, v77
	v_med3_f32 v15, v15, v90, v77
	v_perm_b32 v3, v7, v3, v91
	v_perm_b32 v11, v15, v11, v91
	v_lshl_or_b32 v66, v11, 16, v3
	v_fmamk_f32 v19, v19, 0x44800000, v76
	v_fmamk_f32 v23, v23, 0x44800000, v76
	v_fmamk_f32 v27, v27, 0x44800000, v76
	v_fmamk_f32 v31, v31, 0x44800000, v76
	v_med3_f32 v19, v19, v90, v77
	v_med3_f32 v23, v23, v90, v77
	v_med3_f32 v27, v27, v90, v77
	v_med3_f32 v31, v31, v90, v77
	v_perm_b32 v19, v23, v19, v91
	v_perm_b32 v27, v31, v27, v91
	v_lshl_or_b32 v67, v27, 16, v19
	v_fmamk_f32 v35, v35, 0x44800000, v76
	v_fmamk_f32 v39, v39, 0x44800000, v76
	v_fmamk_f32 v43, v43, 0x44800000, v76
	v_fmamk_f32 v47, v47, 0x44800000, v76
	v_med3_f32 v35, v35, v90, v77
	v_med3_f32 v39, v39, v90, v77
	v_med3_f32 v43, v43, v90, v77
	v_med3_f32 v47, v47, v90, v77
	v_perm_b32 v35, v39, v35, v91
	v_perm_b32 v43, v47, v43, v91
	v_lshl_or_b32 v68, v43, 16, v35
	v_fmamk_f32 v51, v51, 0x44800000, v76
	v_fmamk_f32 v55, v55, 0x44800000, v76
	v_fmamk_f32 v59, v59, 0x44800000, v76
	v_fmamk_f32 v63, v63, 0x44800000, v76
	v_med3_f32 v51, v51, v90, v77
	v_med3_f32 v55, v55, v90, v77
	v_med3_f32 v59, v59, v90, v77
	v_med3_f32 v63, v63, v90, v77
	v_perm_b32 v51, v55, v51, v91
	v_perm_b32 v59, v63, v59, v91
	v_lshl_or_b32 v69, v59, 16, v51
	ds_write_b128 v89, v[66:69] offset:528
	v_fmamk_f32 v4, v4, 0x44800000, v76
	v_fmamk_f32 v8, v8, 0x44800000, v76
	v_fmamk_f32 v12, v12, 0x44800000, v76
	v_fmamk_f32 v16, v16, 0x44800000, v76
	v_med3_f32 v4, v4, v90, v77
	v_med3_f32 v8, v8, v90, v77
	v_med3_f32 v12, v12, v90, v77
	v_med3_f32 v16, v16, v90, v77
	v_perm_b32 v4, v8, v4, v91
	v_perm_b32 v12, v16, v12, v91
	v_lshl_or_b32 v66, v12, 16, v4
	v_fmamk_f32 v20, v20, 0x44800000, v76
	v_fmamk_f32 v24, v24, 0x44800000, v76
	v_fmamk_f32 v28, v28, 0x44800000, v76
	v_fmamk_f32 v32, v32, 0x44800000, v76
	v_med3_f32 v20, v20, v90, v77
	v_med3_f32 v24, v24, v90, v77
	v_med3_f32 v28, v28, v90, v77
	v_med3_f32 v32, v32, v90, v77
	v_perm_b32 v20, v24, v20, v91
	v_perm_b32 v28, v32, v28, v91
	v_lshl_or_b32 v67, v28, 16, v20
	v_fmamk_f32 v36, v36, 0x44800000, v76
	v_fmamk_f32 v40, v40, 0x44800000, v76
	v_fmamk_f32 v44, v44, 0x44800000, v76
	v_fmamk_f32 v48, v48, 0x44800000, v76
	v_med3_f32 v36, v36, v90, v77
	v_med3_f32 v40, v40, v90, v77
	v_med3_f32 v44, v44, v90, v77
	v_med3_f32 v48, v48, v90, v77
	v_perm_b32 v36, v40, v36, v91
	v_perm_b32 v44, v48, v44, v91
	v_lshl_or_b32 v68, v44, 16, v36
	v_fmamk_f32 v52, v52, 0x44800000, v76
	v_fmamk_f32 v56, v56, 0x44800000, v76
	v_fmamk_f32 v60, v60, 0x44800000, v76
	v_fmamk_f32 v64, v64, 0x44800000, v76
	v_med3_f32 v52, v52, v90, v77
	v_med3_f32 v56, v56, v90, v77
	v_med3_f32 v60, v60, v90, v77
	v_med3_f32 v64, v64, v90, v77
	v_perm_b32 v52, v56, v52, v91
	v_perm_b32 v60, v64, v60, v91
	v_lshl_or_b32 v69, v60, 16, v52
	ds_write_b128 v89, v[66:69] offset:1056
	v_fmamk_f32 v5, v5, 0x44800000, v76
	v_fmamk_f32 v9, v9, 0x44800000, v76
	v_fmamk_f32 v13, v13, 0x44800000, v76
	v_fmamk_f32 v17, v17, 0x44800000, v76
	v_med3_f32 v5, v5, v90, v77
	v_med3_f32 v9, v9, v90, v77
	v_med3_f32 v13, v13, v90, v77
	v_med3_f32 v17, v17, v90, v77
	v_perm_b32 v5, v9, v5, v91
	v_perm_b32 v13, v17, v13, v91
	v_lshl_or_b32 v66, v13, 16, v5
	v_fmamk_f32 v21, v21, 0x44800000, v76
	v_fmamk_f32 v25, v25, 0x44800000, v76
	v_fmamk_f32 v29, v29, 0x44800000, v76
	v_fmamk_f32 v33, v33, 0x44800000, v76
	v_med3_f32 v21, v21, v90, v77
	v_med3_f32 v25, v25, v90, v77
	v_med3_f32 v29, v29, v90, v77
	v_med3_f32 v33, v33, v90, v77
	v_perm_b32 v21, v25, v21, v91
	v_perm_b32 v29, v33, v29, v91
	v_lshl_or_b32 v67, v29, 16, v21
	v_fmamk_f32 v37, v37, 0x44800000, v76
	v_fmamk_f32 v41, v41, 0x44800000, v76
	v_fmamk_f32 v45, v45, 0x44800000, v76
	v_fmamk_f32 v49, v49, 0x44800000, v76
	v_med3_f32 v37, v37, v90, v77
	v_med3_f32 v41, v41, v90, v77
	v_med3_f32 v45, v45, v90, v77
	v_med3_f32 v49, v49, v90, v77
	v_perm_b32 v37, v41, v37, v91
	v_perm_b32 v45, v49, v45, v91
	v_lshl_or_b32 v68, v45, 16, v37
	v_fmamk_f32 v53, v53, 0x44800000, v76
	v_fmamk_f32 v57, v57, 0x44800000, v76
	v_fmamk_f32 v61, v61, 0x44800000, v76
	v_fmamk_f32 v65, v65, 0x44800000, v76
	v_med3_f32 v53, v53, v90, v77
	v_med3_f32 v57, v57, v90, v77
	v_med3_f32 v61, v61, v90, v77
	v_med3_f32 v65, v65, v90, v77
	v_perm_b32 v53, v57, v53, v91
	v_perm_b32 v61, v65, v61, v91
	v_lshl_or_b32 v69, v61, 16, v53
	ds_write_b128 v89, v[66:69] offset:1584
	s_mov_b64 s[18:19], 0
